# speedup vs baseline: 1.0048x; 1.0048x over previous
.Lk2_pro:
	s_cmp_le_u32 s22, 16
	s_cselect_b32 s40, s18, 0x1c000
	s_add_u32 m0, s40, s35
	s_add_u32 s22, s22, 1
	global_load_lds_dwordx4 v168, s[20:21]
	global_load_lds_dwordx4 v168, s[20:21] offset:1024
	s_cmp_le_u32 s22, 16
	s_cselect_b32 s41, 0x4000, 0
	s_add_u32 s20, s20, s41
	s_addc_u32 s21, s21, 0
	s_add_u32 s18, s18, 0x4000
	s_cmp_eq_u32 s18, 0x1c000
	s_cselect_b32 s18, 0, s18
	s_cmp_eq_u32 s38, s39
	s_cbranch_scc0 .Lk2_pro_nopsi
	s_add_u32 s14, s14, 1
	s_cmp_eq_u32 s14, 16
	s_cselect_b32 s42, 1, 0
	s_add_u32 s13, s13, s42
	s_cmp_eq_u32 s42, 1
	s_cselect_b32 s14, s13, s14
	s_min_u32 s43, s13, 15
	s_min_u32 s44, s14, 15
	s_lshl_b32 s45, s44, 16
	s_add_u32 s24, s8, s45
	s_addc_u32 s25, s9, 0
	s_add_u32 s26, s24, 0x100000
	s_addc_u32 s27, s25, 0
	s_lshl_b32 s45, s43, 16
	s_add_u32 s28, s8, s45
	s_addc_u32 s29, s9, 0
	s_add_u32 s30, s28, 0x100000
	s_addc_u32 s31, s29, 0
	global_load_dwordx4 v[60:63], v164, s[24:25]
	global_load_dwordx4 v[56:59], v164, s[26:27]
	global_load_dwordx4 v[64:67], v165, s[28:29]
	global_load_dwordx4 v[68:71], v166, s[28:29]
	global_load_dwordx4 v[72:75], v165, s[30:31]
	global_load_dwordx4 v[76:79], v166, s[30:31]
.Lk2_pro_nopsi:
	s_add_u32 s38, s38, 1
	s_cmp_le_u32 s38, 4
	s_cbranch_scc1 .Lk2_pro
	v_mov_b64_e32 v[0:1], 0
	v_mov_b64_e32 v[2:3], 0
	v_mov_b64_e32 v[4:5], 0
	v_mov_b64_e32 v[6:7], 0
	v_mov_b64_e32 v[8:9], 0
	v_mov_b64_e32 v[10:11], 0
	v_mov_b64_e32 v[12:13], 0
	v_mov_b64_e32 v[14:15], 0
	v_mov_b64_e32 v[16:17], 0
	v_mov_b64_e32 v[18:19], 0
	v_mov_b64_e32 v[20:21], 0
	v_mov_b64_e32 v[22:23], 0
	v_mov_b64_e32 v[24:25], 0
	v_mov_b64_e32 v[26:27], 0
	v_mov_b64_e32 v[28:29], 0
	v_mov_b64_e32 v[30:31], 0
	s_cmp_eq_u32 s46, 0
	s_cbranch_scc1 .Lk2_pro_w6
	s_waitcnt vmcnt(10)
	s_branch .Lk2_pro_bar
.Lk2_pro_w6:
	s_waitcnt vmcnt(4)

.Lk2_s00:
	s_bitcmp1_b32 s17, 0
	s_cbranch_scc1 .Lk2_b00
	s_waitcnt vmcnt(4)
	s_barrier
.Lk2_b00:
	s_waitcnt lgkmcnt(4)
	v_mfma_f32_32x32x16_f16 v[16:31], v[144:147], v[80:83], v[16:31]
	s_cmp_le_u32 s22, 16
	s_cselect_b32 s40, s18, 0x1c000
	s_add_u32 m0, s40, s35
	s_add_u32 s22, s22, 1
	global_load_lds_dwordx4 v168, s[20:21]
	global_load_lds_dwordx4 v168, s[20:21] offset:1024
	v_pk_mul_f16 v152, v48, v32 op_sel:[1,0] op_sel_hi:[1,1]
	v_pk_mul_f16 v153, v48, v33 op_sel:[1,0] op_sel_hi:[1,1]
	v_pk_mul_f16 v154, v48, v34 op_sel:[1,0] op_sel_hi:[1,1]
	v_pk_mul_f16 v155, v48, v35 op_sel:[1,0] op_sel_hi:[1,1]
	v_mfma_f32_32x32x16_f16 v[0:15], v[144:147], v[84:87], v[0:15]
	s_cmp_le_u32 s22, 16
	s_cselect_b32 s41, 0x4000, 0
	v_pk_fma_f16 v152, v40, v36, v152 op_sel:[1,0,0] op_sel_hi:[1,1,1]
	v_pk_fma_f16 v153, v40, v37, v153 op_sel:[1,0,0] op_sel_hi:[1,1,1]
	v_pk_fma_f16 v154, v40, v38, v154 op_sel:[1,0,0] op_sel_hi:[1,1,1]
	v_pk_fma_f16 v155, v40, v39, v155 op_sel:[1,0,0] op_sel_hi:[1,1,1]
	v_mfma_f32_32x32x16_f16 v[16:31], v[148:151], v[88:91], v[16:31]
	s_add_u32 s20, s20, s41
	s_addc_u32 s21, s21, 0
	v_pk_mul_f16 v156, v48, v36 op_sel:[1,0] op_sel_hi:[1,1]
	v_pk_mul_f16 v157, v48, v37 op_sel:[1,0] op_sel_hi:[1,1]
	v_pk_mul_f16 v158, v48, v38 op_sel:[1,0] op_sel_hi:[1,1]
	v_pk_mul_f16 v159, v48, v39 op_sel:[1,0] op_sel_hi:[1,1]
	v_mfma_f32_32x32x16_f16 v[0:15], v[148:151], v[92:95], v[0:15]
	s_add_u32 s18, s18, 0x4000
	s_cmp_eq_u32 s18, 0x1c000
	s_cselect_b32 s18, 0, s18
	v_pk_fma_f16 v156, v40, v32, v156 op_sel:[1,0,0] op_sel_hi:[1,1,1] neg_lo:[0,0,1] neg_hi:[0,0,1]
	v_pk_fma_f16 v157, v40, v33, v157 op_sel:[1,0,0] op_sel_hi:[1,1,1] neg_lo:[0,0,1] neg_hi:[0,0,1]
	v_pk_fma_f16 v158, v40, v34, v158 op_sel:[1,0,0] op_sel_hi:[1,1,1] neg_lo:[0,0,1] neg_hi:[0,0,1]
	v_pk_fma_f16 v159, v40, v35, v159 op_sel:[1,0,0] op_sel_hi:[1,1,1] neg_lo:[0,0,1] neg_hi:[0,0,1]
	ds_read_b128 v[112:115], v161 offset:8192
	ds_read_b128 v[116:119], v161 offset:9216
	ds_read_b128 v[120:123], v161 offset:10240
	ds_read_b128 v[124:127], v161 offset:11264
	s_waitcnt lgkmcnt(4)
	v_mfma_f32_32x32x16_f16 v[16:31], v[152:155], v[96:99], v[16:31]
	s_add_u32 s14, s14, 1
	s_cmp_eq_u32 s14, 16
	s_cselect_b32 s42, 1, 0
	v_pk_mul_f16 v144, v49, v32 op_sel:[0,0] op_sel_hi:[0,1]
	v_pk_mul_f16 v145, v49, v33 op_sel:[0,0] op_sel_hi:[0,1]
	v_pk_mul_f16 v146, v49, v34 op_sel:[0,0] op_sel_hi:[0,1]
	v_pk_mul_f16 v147, v49, v35 op_sel:[0,0] op_sel_hi:[0,1]
	v_mfma_f32_32x32x16_f16 v[0:15], v[152:155], v[100:103], v[0:15]
	s_add_u32 s13, s13, s42
	s_cmp_eq_u32 s42, 1
	s_cselect_b32 s14, s13, s14
	v_pk_fma_f16 v144, v41, v36, v144 op_sel:[0,0,0] op_sel_hi:[0,1,1]
	v_pk_fma_f16 v145, v41, v37, v145 op_sel:[0,0,0] op_sel_hi:[0,1,1]
	v_pk_fma_f16 v146, v41, v38, v146 op_sel:[0,0,0] op_sel_hi:[0,1,1]
	v_pk_fma_f16 v147, v41, v39, v147 op_sel:[0,0,0] op_sel_hi:[0,1,1]
	v_mfma_f32_32x32x16_f16 v[16:31], v[156:159], v[104:107], v[16:31]
	s_min_u32 s43, s13, 15
	s_min_u32 s44, s14, 15
	s_lshl_b32 s45, s44, 16
	v_pk_mul_f16 v148, v49, v36 op_sel:[0,0] op_sel_hi:[0,1]
	v_pk_mul_f16 v149, v49, v37 op_sel:[0,0] op_sel_hi:[0,1]
	v_pk_mul_f16 v150, v49, v38 op_sel:[0,0] op_sel_hi:[0,1]
	v_pk_mul_f16 v151, v49, v39 op_sel:[0,0] op_sel_hi:[0,1]
	v_mfma_f32_32x32x16_f16 v[0:15], v[156:159], v[108:111], v[0:15]
	s_add_u32 s24, s8, s45
	s_addc_u32 s25, s9, 0
	v_pk_fma_f16 v148, v41, v32, v148 op_sel:[0,0,0] op_sel_hi:[0,1,1] neg_lo:[0,0,1] neg_hi:[0,0,1]
	v_pk_fma_f16 v149, v41, v33, v149 op_sel:[0,0,0] op_sel_hi:[0,1,1] neg_lo:[0,0,1] neg_hi:[0,0,1]
	v_pk_fma_f16 v150, v41, v34, v150 op_sel:[0,0,0] op_sel_hi:[0,1,1] neg_lo:[0,0,1] neg_hi:[0,0,1]
	v_pk_fma_f16 v151, v41, v35, v151 op_sel:[0,0,0] op_sel_hi:[0,1,1] neg_lo:[0,0,1] neg_hi:[0,0,1]
	ds_read_b128 v[128:131], v161 offset:12288
	ds_read_b128 v[132:135], v161 offset:13312
	ds_read_b128 v[136:139], v161 offset:14336
	ds_read_b128 v[140:143], v161 offset:15360
	s_add_u32 s19, s19, 0x4000
	s_cmp_eq_u32 s19, 0x1c000
	s_cselect_b32 s19, 0, s19
	v_add_u32_e32 v161, s19, v160
	s_waitcnt lgkmcnt(4)
	v_mfma_f32_32x32x16_f16 v[16:31], v[144:147], v[112:115], v[16:31]
	s_add_u32 s26, s24, 0x100000
	s_addc_u32 s27, s25, 0
	s_lshl_b32 s45, s43, 16
	s_add_u32 s28, s8, s45
	s_addc_u32 s29, s9, 0
	v_pk_mul_f16 v152, v49, v32 op_sel:[1,0] op_sel_hi:[1,1]
	v_pk_mul_f16 v153, v49, v33 op_sel:[1,0] op_sel_hi:[1,1]
	v_pk_mul_f16 v154, v49, v34 op_sel:[1,0] op_sel_hi:[1,1]
	v_pk_mul_f16 v155, v49, v35 op_sel:[1,0] op_sel_hi:[1,1]
	v_mfma_f32_32x32x16_f16 v[0:15], v[144:147], v[116:119], v[0:15]
	s_add_u32 s30, s28, 0x100000
	s_addc_u32 s31, s29, 0
	v_pk_fma_f16 v152, v41, v36, v152 op_sel:[1,0,0] op_sel_hi:[1,1,1]
	v_pk_fma_f16 v153, v41, v37, v153 op_sel:[1,0,0] op_sel_hi:[1,1,1]
	v_pk_fma_f16 v154, v41, v38, v154 op_sel:[1,0,0] op_sel_hi:[1,1,1]
	v_pk_fma_f16 v155, v41, v39, v155 op_sel:[1,0,0] op_sel_hi:[1,1,1]
	v_mfma_f32_32x32x16_f16 v[16:31], v[148:151], v[120:123], v[16:31]
	global_load_dwordx4 v[60:63], v164, s[24:25]
	v_pk_mul_f16 v156, v49, v36 op_sel:[1,0] op_sel_hi:[1,1]
	v_pk_mul_f16 v157, v49, v37 op_sel:[1,0] op_sel_hi:[1,1]
	v_pk_mul_f16 v158, v49, v38 op_sel:[1,0] op_sel_hi:[1,1]
	v_pk_mul_f16 v159, v49, v39 op_sel:[1,0] op_sel_hi:[1,1]
	v_mfma_f32_32x32x16_f16 v[0:15], v[148:151], v[124:127], v[0:15]
	global_load_dwordx4 v[56:59], v164, s[26:27]
	v_pk_fma_f16 v156, v41, v32, v156 op_sel:[1,0,0] op_sel_hi:[1,1,1] neg_lo:[0,0,1] neg_hi:[0,0,1]
	v_pk_fma_f16 v157, v41, v33, v157 op_sel:[1,0,0] op_sel_hi:[1,1,1] neg_lo:[0,0,1] neg_hi:[0,0,1]
	v_pk_fma_f16 v158, v41, v34, v158 op_sel:[1,0,0] op_sel_hi:[1,1,1] neg_lo:[0,0,1] neg_hi:[0,0,1]
	v_pk_fma_f16 v159, v41, v35, v159 op_sel:[1,0,0] op_sel_hi:[1,1,1] neg_lo:[0,0,1] neg_hi:[0,0,1]
	ds_read_b128 v[80:83], v161
	ds_read_b128 v[84:87], v161 offset:1024
	ds_read_b128 v[88:91], v161 offset:2048
	ds_read_b128 v[92:95], v161 offset:3072
	s_waitcnt lgkmcnt(4)
	v_mfma_f32_32x32x16_f16 v[16:31], v[152:155], v[128:131], v[16:31]
	global_load_dwordx4 v[64:67], v165, s[28:29]
	v_pk_mul_f16 v144, v50, v32 op_sel:[0,0] op_sel_hi:[0,1]
	v_pk_mul_f16 v145, v50, v33 op_sel:[0,0] op_sel_hi:[0,1]
	v_pk_mul_f16 v146, v50, v34 op_sel:[0,0] op_sel_hi:[0,1]
	v_pk_mul_f16 v147, v50, v35 op_sel:[0,0] op_sel_hi:[0,1]
	v_mfma_f32_32x32x16_f16 v[0:15], v[152:155], v[132:135], v[0:15]
	global_load_dwordx4 v[68:71], v166, s[28:29]
	v_pk_fma_f16 v144, v42, v36, v144 op_sel:[0,0,0] op_sel_hi:[0,1,1]
	v_pk_fma_f16 v145, v42, v37, v145 op_sel:[0,0,0] op_sel_hi:[0,1,1]
	v_pk_fma_f16 v146, v42, v38, v146 op_sel:[0,0,0] op_sel_hi:[0,1,1]
	v_pk_fma_f16 v147, v42, v39, v147 op_sel:[0,0,0] op_sel_hi:[0,1,1]
	v_mfma_f32_32x32x16_f16 v[16:31], v[156:159], v[136:139], v[16:31]
	global_load_dwordx4 v[72:75], v165, s[30:31]
	v_pk_mul_f16 v148, v50, v36 op_sel:[0,0] op_sel_hi:[0,1]
	v_pk_mul_f16 v149, v50, v37 op_sel:[0,0] op_sel_hi:[0,1]
	v_pk_mul_f16 v150, v50, v38 op_sel:[0,0] op_sel_hi:[0,1]
	v_pk_mul_f16 v151, v50, v39 op_sel:[0,0] op_sel_hi:[0,1]
	v_mfma_f32_32x32x16_f16 v[0:15], v[156:159], v[140:143], v[0:15]
	global_load_dwordx4 v[76:79], v166, s[30:31]
	v_pk_fma_f16 v148, v42, v32, v148 op_sel:[0,0,0] op_sel_hi:[0,1,1] neg_lo:[0,0,1] neg_hi:[0,0,1]
	v_pk_fma_f16 v149, v42, v33, v149 op_sel:[0,0,0] op_sel_hi:[0,1,1] neg_lo:[0,0,1] neg_hi:[0,0,1]
	v_pk_fma_f16 v150, v42, v34, v150 op_sel:[0,0,0] op_sel_hi:[0,1,1] neg_lo:[0,0,1] neg_hi:[0,0,1]
	v_pk_fma_f16 v151, v42, v35, v151 op_sel:[0,0,0] op_sel_hi:[0,1,1] neg_lo:[0,0,1] neg_hi:[0,0,1]
	ds_read_b128 v[96:99], v161 offset:4096
	ds_read_b128 v[100:103], v161 offset:5120
	ds_read_b128 v[104:107], v161 offset:6144
	ds_read_b128 v[108:111], v161 offset:7168
	s_add_u32 s17, s17, 1
	s_cmp_eq_u32 s17, 17
	s_cbranch_scc1 .Lk2_epi
.Lk2_s01:
	s_bitcmp1_b32 s17, 0
	s_cbranch_scc1 .Lk2_b01
	s_waitcnt vmcnt(10)
	s_barrier
.Lk2_b01:
	s_waitcnt lgkmcnt(4)
	v_mfma_f32_32x32x16_f16 v[16:31], v[144:147], v[80:83], v[16:31]
	s_cmp_le_u32 s22, 16
	s_cselect_b32 s40, s18, 0x1c000
	s_add_u32 m0, s40, s35
	v_pk_mul_f16 v152, v50, v32 op_sel:[1,0] op_sel_hi:[1,1]
	v_pk_mul_f16 v153, v50, v33 op_sel:[1,0] op_sel_hi:[1,1]
	v_pk_mul_f16 v154, v50, v34 op_sel:[1,0] op_sel_hi:[1,1]
	v_pk_mul_f16 v155, v50, v35 op_sel:[1,0] op_sel_hi:[1,1]
	v_mfma_f32_32x32x16_f16 v[0:15], v[144:147], v[84:87], v[0:15]
	s_add_u32 s22, s22, 1
	global_load_lds_dwordx4 v168, s[20:21]
	global_load_lds_dwordx4 v168, s[20:21] offset:1024
	v_pk_fma_f16 v152, v42, v36, v152 op_sel:[1,0,0] op_sel_hi:[1,1,1]
	v_pk_fma_f16 v153, v42, v37, v153 op_sel:[1,0,0] op_sel_hi:[1,1,1]
	v_pk_fma_f16 v154, v42, v38, v154 op_sel:[1,0,0] op_sel_hi:[1,1,1]
	v_pk_fma_f16 v155, v42, v39, v155 op_sel:[1,0,0] op_sel_hi:[1,1,1]
	v_mfma_f32_32x32x16_f16 v[16:31], v[148:151], v[88:91], v[16:31]
	s_cmp_le_u32 s22, 16
	s_cselect_b32 s41, 0x4000, 0
	v_pk_mul_f16 v156, v50, v36 op_sel:[1,0] op_sel_hi:[1,1]
	v_pk_mul_f16 v157, v50, v37 op_sel:[1,0] op_sel_hi:[1,1]
	v_pk_mul_f16 v158, v50, v38 op_sel:[1,0] op_sel_hi:[1,1]
	v_pk_mul_f16 v159, v50, v39 op_sel:[1,0] op_sel_hi:[1,1]
	v_mfma_f32_32x32x16_f16 v[0:15], v[148:151], v[92:95], v[0:15]
	s_add_u32 s20, s20, s41
	s_addc_u32 s21, s21, 0
	v_pk_fma_f16 v156, v42, v32, v156 op_sel:[1,0,0] op_sel_hi:[1,1,1] neg_lo:[0,0,1] neg_hi:[0,0,1]
	v_pk_fma_f16 v157, v42, v33, v157 op_sel:[1,0,0] op_sel_hi:[1,1,1] neg_lo:[0,0,1] neg_hi:[0,0,1]
	v_pk_fma_f16 v158, v42, v34, v158 op_sel:[1,0,0] op_sel_hi:[1,1,1] neg_lo:[0,0,1] neg_hi:[0,0,1]
	v_pk_fma_f16 v159, v42, v35, v159 op_sel:[1,0,0] op_sel_hi:[1,1,1] neg_lo:[0,0,1] neg_hi:[0,0,1]
	ds_read_b128 v[112:115], v161 offset:8192
	ds_read_b128 v[116:119], v161 offset:9216
	ds_read_b128 v[120:123], v161 offset:10240
	ds_read_b128 v[124:127], v161 offset:11264
	s_waitcnt lgkmcnt(4)
	v_mfma_f32_32x32x16_f16 v[16:31], v[152:155], v[96:99], v[16:31]
	s_add_u32 s18, s18, 0x4000
	s_cmp_eq_u32 s18, 0x1c000
	s_cselect_b32 s18, 0, s18
	v_pk_mul_f16 v144, v51, v32 op_sel:[0,0] op_sel_hi:[0,1]
	v_pk_mul_f16 v145, v51, v33 op_sel:[0,0] op_sel_hi:[0,1]
	v_pk_mul_f16 v146, v51, v34 op_sel:[0,0] op_sel_hi:[0,1]
	v_pk_mul_f16 v147, v51, v35 op_sel:[0,0] op_sel_hi:[0,1]
	v_mfma_f32_32x32x16_f16 v[0:15], v[152:155], v[100:103], v[0:15]
	v_pk_fma_f16 v144, v43, v36, v144 op_sel:[0,0,0] op_sel_hi:[0,1,1]
	v_pk_fma_f16 v145, v43, v37, v145 op_sel:[0,0,0] op_sel_hi:[0,1,1]
	v_pk_fma_f16 v146, v43, v38, v146 op_sel:[0,0,0] op_sel_hi:[0,1,1]
	v_pk_fma_f16 v147, v43, v39, v147 op_sel:[0,0,0] op_sel_hi:[0,1,1]
	v_mfma_f32_32x32x16_f16 v[16:31], v[156:159], v[104:107], v[16:31]
	v_pk_mul_f16 v148, v51, v36 op_sel:[0,0] op_sel_hi:[0,1]
	v_pk_mul_f16 v149, v51, v37 op_sel:[0,0] op_sel_hi:[0,1]
	v_pk_mul_f16 v150, v51, v38 op_sel:[0,0] op_sel_hi:[0,1]
	v_pk_mul_f16 v151, v51, v39 op_sel:[0,0] op_sel_hi:[0,1]
	v_mfma_f32_32x32x16_f16 v[0:15], v[156:159], v[108:111], v[0:15]
	v_pk_fma_f16 v148, v43, v32, v148 op_sel:[0,0,0] op_sel_hi:[0,1,1] neg_lo:[0,0,1] neg_hi:[0,0,1]
	v_pk_fma_f16 v149, v43, v33, v149 op_sel:[0,0,0] op_sel_hi:[0,1,1] neg_lo:[0,0,1] neg_hi:[0,0,1]
	v_pk_fma_f16 v150, v43, v34, v150 op_sel:[0,0,0] op_sel_hi:[0,1,1] neg_lo:[0,0,1] neg_hi:[0,0,1]
	v_pk_fma_f16 v151, v43, v35, v151 op_sel:[0,0,0] op_sel_hi:[0,1,1] neg_lo:[0,0,1] neg_hi:[0,0,1]
	ds_read_b128 v[128:131], v161 offset:12288
	ds_read_b128 v[132:135], v161 offset:13312
	ds_read_b128 v[136:139], v161 offset:14336
	ds_read_b128 v[140:143], v161 offset:15360
	s_add_u32 s19, s19, 0x4000
	s_cmp_eq_u32 s19, 0x1c000
	s_cselect_b32 s19, 0, s19
	v_add_u32_e32 v161, s19, v160
	s_waitcnt lgkmcnt(4)
	v_mfma_f32_32x32x16_f16 v[16:31], v[144:147], v[112:115], v[16:31]
	v_pk_mul_f16 v152, v51, v32 op_sel:[1,0] op_sel_hi:[1,1]
	v_pk_mul_f16 v153, v51, v33 op_sel:[1,0] op_sel_hi:[1,1]
	v_pk_mul_f16 v154, v51, v34 op_sel:[1,0] op_sel_hi:[1,1]
	v_pk_mul_f16 v155, v51, v35 op_sel:[1,0] op_sel_hi:[1,1]
	v_mfma_f32_32x32x16_f16 v[0:15], v[144:147], v[116:119], v[0:15]
	v_pk_fma_f16 v152, v43, v36, v152 op_sel:[1,0,0] op_sel_hi:[1,1,1]
	v_pk_fma_f16 v153, v43, v37, v153 op_sel:[1,0,0] op_sel_hi:[1,1,1]
	v_pk_fma_f16 v154, v43, v38, v154 op_sel:[1,0,0] op_sel_hi:[1,1,1]
	v_pk_fma_f16 v155, v43, v39, v155 op_sel:[1,0,0] op_sel_hi:[1,1,1]
	v_mfma_f32_32x32x16_f16 v[16:31], v[148:151], v[120:123], v[16:31]
	v_pk_mul_f16 v156, v51, v36 op_sel:[1,0] op_sel_hi:[1,1]
	v_pk_mul_f16 v157, v51, v37 op_sel:[1,0] op_sel_hi:[1,1]
	v_pk_mul_f16 v158, v51, v38 op_sel:[1,0] op_sel_hi:[1,1]
	v_pk_mul_f16 v159, v51, v39 op_sel:[1,0] op_sel_hi:[1,1]
	v_mfma_f32_32x32x16_f16 v[0:15], v[148:151], v[124:127], v[0:15]
	v_pk_fma_f16 v156, v43, v32, v156 op_sel:[1,0,0] op_sel_hi:[1,1,1] neg_lo:[0,0,1] neg_hi:[0,0,1]
	v_pk_fma_f16 v157, v43, v33, v157 op_sel:[1,0,0] op_sel_hi:[1,1,1] neg_lo:[0,0,1] neg_hi:[0,0,1]
	v_pk_fma_f16 v158, v43, v34, v158 op_sel:[1,0,0] op_sel_hi:[1,1,1] neg_lo:[0,0,1] neg_hi:[0,0,1]
	v_pk_fma_f16 v159, v43, v35, v159 op_sel:[1,0,0] op_sel_hi:[1,1,1] neg_lo:[0,0,1] neg_hi:[0,0,1]
	ds_read_b128 v[80:83], v161
	ds_read_b128 v[84:87], v161 offset:1024
	ds_read_b128 v[88:91], v161 offset:2048
	ds_read_b128 v[92:95], v161 offset:3072
	s_waitcnt lgkmcnt(4)
	v_mfma_f32_32x32x16_f16 v[16:31], v[152:155], v[128:131], v[16:31]
	v_pk_mul_f16 v144, v52, v32 op_sel:[0,0] op_sel_hi:[0,1]
	v_pk_mul_f16 v145, v52, v33 op_sel:[0,0] op_sel_hi:[0,1]
	v_pk_mul_f16 v146, v52, v34 op_sel:[0,0] op_sel_hi:[0,1]
	v_pk_mul_f16 v147, v52, v35 op_sel:[0,0] op_sel_hi:[0,1]
	v_mfma_f32_32x32x16_f16 v[0:15], v[152:155], v[132:135], v[0:15]
	v_pk_fma_f16 v144, v44, v36, v144 op_sel:[0,0,0] op_sel_hi:[0,1,1]
	v_pk_fma_f16 v145, v44, v37, v145 op_sel:[0,0,0] op_sel_hi:[0,1,1]
	v_pk_fma_f16 v146, v44, v38, v146 op_sel:[0,0,0] op_sel_hi:[0,1,1]
	v_pk_fma_f16 v147, v44, v39, v147 op_sel:[0,0,0] op_sel_hi:[0,1,1]
	v_mfma_f32_32x32x16_f16 v[16:31], v[156:159], v[136:139], v[16:31]
	v_pk_mul_f16 v148, v52, v36 op_sel:[0,0] op_sel_hi:[0,1]
	v_pk_mul_f16 v149, v52, v37 op_sel:[0,0] op_sel_hi:[0,1]
	v_pk_mul_f16 v150, v52, v38 op_sel:[0,0] op_sel_hi:[0,1]
	v_pk_mul_f16 v151, v52, v39 op_sel:[0,0] op_sel_hi:[0,1]
	v_mfma_f32_32x32x16_f16 v[0:15], v[156:159], v[140:143], v[0:15]
	v_pk_fma_f16 v148, v44, v32, v148 op_sel:[0,0,0] op_sel_hi:[0,1,1] neg_lo:[0,0,1] neg_hi:[0,0,1]
	v_pk_fma_f16 v149, v44, v33, v149 op_sel:[0,0,0] op_sel_hi:[0,1,1] neg_lo:[0,0,1] neg_hi:[0,0,1]
	v_pk_fma_f16 v150, v44, v34, v150 op_sel:[0,0,0] op_sel_hi:[0,1,1] neg_lo:[0,0,1] neg_hi:[0,0,1]
	v_pk_fma_f16 v151, v44, v35, v151 op_sel:[0,0,0] op_sel_hi:[0,1,1] neg_lo:[0,0,1] neg_hi:[0,0,1]
	ds_read_b128 v[96:99], v161 offset:4096
	ds_read_b128 v[100:103], v161 offset:5120
	ds_read_b128 v[104:107], v161 offset:6144
	ds_read_b128 v[108:111], v161 offset:7168
	s_add_u32 s17, s17, 1
	s_cmp_eq_u32 s17, 17
	s_cbranch_scc1 .Lk2_epi

.Lk2_b02:
	s_waitcnt lgkmcnt(4)
	v_mfma_f32_32x32x16_f16 v[16:31], v[144:147], v[80:83], v[16:31]
	s_cmp_le_u32 s22, 16
	s_cselect_b32 s40, s18, 0x1c000
	s_add_u32 m0, s40, s35
	v_pk_mul_f16 v152, v52, v32 op_sel:[1,0] op_sel_hi:[1,1]
	v_pk_mul_f16 v153, v52, v33 op_sel:[1,0] op_sel_hi:[1,1]
	v_pk_mul_f16 v154, v52, v34 op_sel:[1,0] op_sel_hi:[1,1]
	v_pk_mul_f16 v155, v52, v35 op_sel:[1,0] op_sel_hi:[1,1]
	v_mfma_f32_32x32x16_f16 v[0:15], v[144:147], v[84:87], v[0:15]
	s_add_u32 s22, s22, 1
	global_load_lds_dwordx4 v168, s[20:21]
	global_load_lds_dwordx4 v168, s[20:21] offset:1024
	v_pk_fma_f16 v152, v44, v36, v152 op_sel:[1,0,0] op_sel_hi:[1,1,1]
	v_pk_fma_f16 v153, v44, v37, v153 op_sel:[1,0,0] op_sel_hi:[1,1,1]
	v_pk_fma_f16 v154, v44, v38, v154 op_sel:[1,0,0] op_sel_hi:[1,1,1]
	v_pk_fma_f16 v155, v44, v39, v155 op_sel:[1,0,0] op_sel_hi:[1,1,1]
	v_mfma_f32_32x32x16_f16 v[16:31], v[148:151], v[88:91], v[16:31]
	s_cmp_le_u32 s22, 16
	s_cselect_b32 s41, 0x4000, 0
	v_pk_mul_f16 v156, v52, v36 op_sel:[1,0] op_sel_hi:[1,1]
	v_pk_mul_f16 v157, v52, v37 op_sel:[1,0] op_sel_hi:[1,1]
	v_pk_mul_f16 v158, v52, v38 op_sel:[1,0] op_sel_hi:[1,1]
	v_pk_mul_f16 v159, v52, v39 op_sel:[1,0] op_sel_hi:[1,1]
	v_mfma_f32_32x32x16_f16 v[0:15], v[148:151], v[92:95], v[0:15]
	s_add_u32 s20, s20, s41
	s_addc_u32 s21, s21, 0
	v_pk_fma_f16 v156, v44, v32, v156 op_sel:[1,0,0] op_sel_hi:[1,1,1] neg_lo:[0,0,1] neg_hi:[0,0,1]
	v_pk_fma_f16 v157, v44, v33, v157 op_sel:[1,0,0] op_sel_hi:[1,1,1] neg_lo:[0,0,1] neg_hi:[0,0,1]
	v_pk_fma_f16 v158, v44, v34, v158 op_sel:[1,0,0] op_sel_hi:[1,1,1] neg_lo:[0,0,1] neg_hi:[0,0,1]
	v_pk_fma_f16 v159, v44, v35, v159 op_sel:[1,0,0] op_sel_hi:[1,1,1] neg_lo:[0,0,1] neg_hi:[0,0,1]
	ds_read_b128 v[112:115], v161 offset:8192
	ds_read_b128 v[116:119], v161 offset:9216
	ds_read_b128 v[120:123], v161 offset:10240
	ds_read_b128 v[124:127], v161 offset:11264
	s_waitcnt lgkmcnt(4)
	v_mfma_f32_32x32x16_f16 v[16:31], v[152:155], v[96:99], v[16:31]
	s_add_u32 s18, s18, 0x4000
	s_cmp_eq_u32 s18, 0x1c000
	s_cselect_b32 s18, 0, s18
	v_pk_mul_f16 v144, v53, v32 op_sel:[0,0] op_sel_hi:[0,1]
	v_pk_mul_f16 v145, v53, v33 op_sel:[0,0] op_sel_hi:[0,1]
	v_pk_mul_f16 v146, v53, v34 op_sel:[0,0] op_sel_hi:[0,1]
	v_pk_mul_f16 v147, v53, v35 op_sel:[0,0] op_sel_hi:[0,1]
	v_mfma_f32_32x32x16_f16 v[0:15], v[152:155], v[100:103], v[0:15]
	v_pk_fma_f16 v144, v45, v36, v144 op_sel:[0,0,0] op_sel_hi:[0,1,1]
	v_pk_fma_f16 v145, v45, v37, v145 op_sel:[0,0,0] op_sel_hi:[0,1,1]
	v_pk_fma_f16 v146, v45, v38, v146 op_sel:[0,0,0] op_sel_hi:[0,1,1]
	v_pk_fma_f16 v147, v45, v39, v147 op_sel:[0,0,0] op_sel_hi:[0,1,1]
	v_mfma_f32_32x32x16_f16 v[16:31], v[156:159], v[104:107], v[16:31]
	v_pk_mul_f16 v148, v53, v36 op_sel:[0,0] op_sel_hi:[0,1]
	v_pk_mul_f16 v149, v53, v37 op_sel:[0,0] op_sel_hi:[0,1]
	v_pk_mul_f16 v150, v53, v38 op_sel:[0,0] op_sel_hi:[0,1]
	v_pk_mul_f16 v151, v53, v39 op_sel:[0,0] op_sel_hi:[0,1]
	v_mfma_f32_32x32x16_f16 v[0:15], v[156:159], v[108:111], v[0:15]
	v_pk_fma_f16 v148, v45, v32, v148 op_sel:[0,0,0] op_sel_hi:[0,1,1] neg_lo:[0,0,1] neg_hi:[0,0,1]
	v_pk_fma_f16 v149, v45, v33, v149 op_sel:[0,0,0] op_sel_hi:[0,1,1] neg_lo:[0,0,1] neg_hi:[0,0,1]
	v_pk_fma_f16 v150, v45, v34, v150 op_sel:[0,0,0] op_sel_hi:[0,1,1] neg_lo:[0,0,1] neg_hi:[0,0,1]
	v_pk_fma_f16 v151, v45, v35, v151 op_sel:[0,0,0] op_sel_hi:[0,1,1] neg_lo:[0,0,1] neg_hi:[0,0,1]
	ds_read_b128 v[128:131], v161 offset:12288
	ds_read_b128 v[132:135], v161 offset:13312
	ds_read_b128 v[136:139], v161 offset:14336
	ds_read_b128 v[140:143], v161 offset:15360
	s_add_u32 s19, s19, 0x4000
	s_cmp_eq_u32 s19, 0x1c000
	s_cselect_b32 s19, 0, s19
	v_add_u32_e32 v161, s19, v160
	s_waitcnt lgkmcnt(4)
	v_mfma_f32_32x32x16_f16 v[16:31], v[144:147], v[112:115], v[16:31]
	v_pk_mul_f16 v152, v53, v32 op_sel:[1,0] op_sel_hi:[1,1]
	v_pk_mul_f16 v153, v53, v33 op_sel:[1,0] op_sel_hi:[1,1]
	v_pk_mul_f16 v154, v53, v34 op_sel:[1,0] op_sel_hi:[1,1]
	v_pk_mul_f16 v155, v53, v35 op_sel:[1,0] op_sel_hi:[1,1]
	v_mfma_f32_32x32x16_f16 v[0:15], v[144:147], v[116:119], v[0:15]
	v_pk_fma_f16 v152, v45, v36, v152 op_sel:[1,0,0] op_sel_hi:[1,1,1]
	v_pk_fma_f16 v153, v45, v37, v153 op_sel:[1,0,0] op_sel_hi:[1,1,1]
	v_pk_fma_f16 v154, v45, v38, v154 op_sel:[1,0,0] op_sel_hi:[1,1,1]
	v_pk_fma_f16 v155, v45, v39, v155 op_sel:[1,0,0] op_sel_hi:[1,1,1]
	v_mfma_f32_32x32x16_f16 v[16:31], v[148:151], v[120:123], v[16:31]
	v_pk_mul_f16 v156, v53, v36 op_sel:[1,0] op_sel_hi:[1,1]
	v_pk_mul_f16 v157, v53, v37 op_sel:[1,0] op_sel_hi:[1,1]
	v_pk_mul_f16 v158, v53, v38 op_sel:[1,0] op_sel_hi:[1,1]
	v_pk_mul_f16 v159, v53, v39 op_sel:[1,0] op_sel_hi:[1,1]
	v_mfma_f32_32x32x16_f16 v[0:15], v[148:151], v[124:127], v[0:15]
	v_pk_fma_f16 v156, v45, v32, v156 op_sel:[1,0,0] op_sel_hi:[1,1,1] neg_lo:[0,0,1] neg_hi:[0,0,1]
	v_pk_fma_f16 v157, v45, v33, v157 op_sel:[1,0,0] op_sel_hi:[1,1,1] neg_lo:[0,0,1] neg_hi:[0,0,1]
	v_pk_fma_f16 v158, v45, v34, v158 op_sel:[1,0,0] op_sel_hi:[1,1,1] neg_lo:[0,0,1] neg_hi:[0,0,1]
	v_pk_fma_f16 v159, v45, v35, v159 op_sel:[1,0,0] op_sel_hi:[1,1,1] neg_lo:[0,0,1] neg_hi:[0,0,1]
	ds_read_b128 v[80:83], v161
	ds_read_b128 v[84:87], v161 offset:1024
	ds_read_b128 v[88:91], v161 offset:2048
	ds_read_b128 v[92:95], v161 offset:3072
	s_waitcnt lgkmcnt(4)
	v_mfma_f32_32x32x16_f16 v[16:31], v[152:155], v[128:131], v[16:31]
	v_pk_mul_f16 v144, v54, v32 op_sel:[0,0] op_sel_hi:[0,1]
	v_pk_mul_f16 v145, v54, v33 op_sel:[0,0] op_sel_hi:[0,1]
	v_pk_mul_f16 v146, v54, v34 op_sel:[0,0] op_sel_hi:[0,1]
	v_pk_mul_f16 v147, v54, v35 op_sel:[0,0] op_sel_hi:[0,1]
	v_mfma_f32_32x32x16_f16 v[0:15], v[152:155], v[132:135], v[0:15]
	v_pk_fma_f16 v144, v46, v36, v144 op_sel:[0,0,0] op_sel_hi:[0,1,1]
	v_pk_fma_f16 v145, v46, v37, v145 op_sel:[0,0,0] op_sel_hi:[0,1,1]
	v_pk_fma_f16 v146, v46, v38, v146 op_sel:[0,0,0] op_sel_hi:[0,1,1]
	v_pk_fma_f16 v147, v46, v39, v147 op_sel:[0,0,0] op_sel_hi:[0,1,1]
	v_mfma_f32_32x32x16_f16 v[16:31], v[156:159], v[136:139], v[16:31]
	v_pk_mul_f16 v148, v54, v36 op_sel:[0,0] op_sel_hi:[0,1]
	v_pk_mul_f16 v149, v54, v37 op_sel:[0,0] op_sel_hi:[0,1]
	v_pk_mul_f16 v150, v54, v38 op_sel:[0,0] op_sel_hi:[0,1]
	v_pk_mul_f16 v151, v54, v39 op_sel:[0,0] op_sel_hi:[0,1]
	v_mfma_f32_32x32x16_f16 v[0:15], v[156:159], v[140:143], v[0:15]
	v_pk_fma_f16 v148, v46, v32, v148 op_sel:[0,0,0] op_sel_hi:[0,1,1] neg_lo:[0,0,1] neg_hi:[0,0,1]
	v_pk_fma_f16 v149, v46, v33, v149 op_sel:[0,0,0] op_sel_hi:[0,1,1] neg_lo:[0,0,1] neg_hi:[0,0,1]
	v_pk_fma_f16 v150, v46, v34, v150 op_sel:[0,0,0] op_sel_hi:[0,1,1] neg_lo:[0,0,1] neg_hi:[0,0,1]
	v_pk_fma_f16 v151, v46, v35, v151 op_sel:[0,0,0] op_sel_hi:[0,1,1] neg_lo:[0,0,1] neg_hi:[0,0,1]
	ds_read_b128 v[96:99], v161 offset:4096
	ds_read_b128 v[100:103], v161 offset:5120
	ds_read_b128 v[104:107], v161 offset:6144
	ds_read_b128 v[108:111], v161 offset:7168
	s_add_u32 s17, s17, 1
	s_cmp_eq_u32 s17, 17
	s_cbranch_scc1 .Lk2_epi

.Lk2_b03:
	s_waitcnt lgkmcnt(4)
	v_mfma_f32_32x32x16_f16 v[16:31], v[144:147], v[80:83], v[16:31]
	s_cmp_le_u32 s22, 16
	s_cselect_b32 s40, s18, 0x1c000
	s_add_u32 m0, s40, s35
	v_pk_mul_f16 v152, v54, v32 op_sel:[1,0] op_sel_hi:[1,1]
	v_pk_mul_f16 v153, v54, v33 op_sel:[1,0] op_sel_hi:[1,1]
	v_pk_mul_f16 v154, v54, v34 op_sel:[1,0] op_sel_hi:[1,1]
	v_pk_mul_f16 v155, v54, v35 op_sel:[1,0] op_sel_hi:[1,1]
	v_mfma_f32_32x32x16_f16 v[0:15], v[144:147], v[84:87], v[0:15]
	s_add_u32 s22, s22, 1
	global_load_lds_dwordx4 v168, s[20:21]
	global_load_lds_dwordx4 v168, s[20:21] offset:1024
	v_pk_fma_f16 v152, v46, v36, v152 op_sel:[1,0,0] op_sel_hi:[1,1,1]
	v_pk_fma_f16 v153, v46, v37, v153 op_sel:[1,0,0] op_sel_hi:[1,1,1]
	v_pk_fma_f16 v154, v46, v38, v154 op_sel:[1,0,0] op_sel_hi:[1,1,1]
	v_pk_fma_f16 v155, v46, v39, v155 op_sel:[1,0,0] op_sel_hi:[1,1,1]
	v_mfma_f32_32x32x16_f16 v[16:31], v[148:151], v[88:91], v[16:31]
	s_cmp_le_u32 s22, 16
	s_cselect_b32 s41, 0x4000, 0
	v_pk_mul_f16 v156, v54, v36 op_sel:[1,0] op_sel_hi:[1,1]
	v_pk_mul_f16 v157, v54, v37 op_sel:[1,0] op_sel_hi:[1,1]
	v_pk_mul_f16 v158, v54, v38 op_sel:[1,0] op_sel_hi:[1,1]
	v_pk_mul_f16 v159, v54, v39 op_sel:[1,0] op_sel_hi:[1,1]
	v_mfma_f32_32x32x16_f16 v[0:15], v[148:151], v[92:95], v[0:15]
	s_add_u32 s20, s20, s41
	s_addc_u32 s21, s21, 0
	v_pk_fma_f16 v156, v46, v32, v156 op_sel:[1,0,0] op_sel_hi:[1,1,1] neg_lo:[0,0,1] neg_hi:[0,0,1]
	v_pk_fma_f16 v157, v46, v33, v157 op_sel:[1,0,0] op_sel_hi:[1,1,1] neg_lo:[0,0,1] neg_hi:[0,0,1]
	v_pk_fma_f16 v158, v46, v34, v158 op_sel:[1,0,0] op_sel_hi:[1,1,1] neg_lo:[0,0,1] neg_hi:[0,0,1]
	v_pk_fma_f16 v159, v46, v35, v159 op_sel:[1,0,0] op_sel_hi:[1,1,1] neg_lo:[0,0,1] neg_hi:[0,0,1]
	ds_read_b128 v[112:115], v161 offset:8192
	ds_read_b128 v[116:119], v161 offset:9216
	ds_read_b128 v[120:123], v161 offset:10240
	ds_read_b128 v[124:127], v161 offset:11264
	s_waitcnt lgkmcnt(4)
	v_mfma_f32_32x32x16_f16 v[16:31], v[152:155], v[96:99], v[16:31]
	s_add_u32 s18, s18, 0x4000
	s_cmp_eq_u32 s18, 0x1c000
	s_cselect_b32 s18, 0, s18
	v_pk_mul_f16 v144, v55, v32 op_sel:[0,0] op_sel_hi:[0,1]
	v_pk_mul_f16 v145, v55, v33 op_sel:[0,0] op_sel_hi:[0,1]
	v_pk_mul_f16 v146, v55, v34 op_sel:[0,0] op_sel_hi:[0,1]
	v_pk_mul_f16 v147, v55, v35 op_sel:[0,0] op_sel_hi:[0,1]
	v_mfma_f32_32x32x16_f16 v[0:15], v[152:155], v[100:103], v[0:15]
	v_pk_fma_f16 v144, v47, v36, v144 op_sel:[0,0,0] op_sel_hi:[0,1,1]
	v_pk_fma_f16 v145, v47, v37, v145 op_sel:[0,0,0] op_sel_hi:[0,1,1]
	v_pk_fma_f16 v146, v47, v38, v146 op_sel:[0,0,0] op_sel_hi:[0,1,1]
	v_pk_fma_f16 v147, v47, v39, v147 op_sel:[0,0,0] op_sel_hi:[0,1,1]
	v_mfma_f32_32x32x16_f16 v[16:31], v[156:159], v[104:107], v[16:31]
	v_pk_mul_f16 v148, v55, v36 op_sel:[0,0] op_sel_hi:[0,1]
	v_pk_mul_f16 v149, v55, v37 op_sel:[0,0] op_sel_hi:[0,1]
	v_pk_mul_f16 v150, v55, v38 op_sel:[0,0] op_sel_hi:[0,1]
	v_pk_mul_f16 v151, v55, v39 op_sel:[0,0] op_sel_hi:[0,1]
	v_mfma_f32_32x32x16_f16 v[0:15], v[156:159], v[108:111], v[0:15]
	v_pk_fma_f16 v148, v47, v32, v148 op_sel:[0,0,0] op_sel_hi:[0,1,1] neg_lo:[0,0,1] neg_hi:[0,0,1]
	v_pk_fma_f16 v149, v47, v33, v149 op_sel:[0,0,0] op_sel_hi:[0,1,1] neg_lo:[0,0,1] neg_hi:[0,0,1]
	v_pk_fma_f16 v150, v47, v34, v150 op_sel:[0,0,0] op_sel_hi:[0,1,1] neg_lo:[0,0,1] neg_hi:[0,0,1]
	v_pk_fma_f16 v151, v47, v35, v151 op_sel:[0,0,0] op_sel_hi:[0,1,1] neg_lo:[0,0,1] neg_hi:[0,0,1]
	ds_read_b128 v[128:131], v161 offset:12288
	ds_read_b128 v[132:135], v161 offset:13312
	ds_read_b128 v[136:139], v161 offset:14336
	ds_read_b128 v[140:143], v161 offset:15360
	s_add_u32 s19, s19, 0x4000
	s_cmp_eq_u32 s19, 0x1c000
	s_cselect_b32 s19, 0, s19
	v_add_u32_e32 v161, s19, v160
	s_waitcnt lgkmcnt(4)
	v_mfma_f32_32x32x16_f16 v[16:31], v[144:147], v[112:115], v[16:31]
	v_pk_mul_f16 v152, v55, v32 op_sel:[1,0] op_sel_hi:[1,1]
	v_pk_mul_f16 v153, v55, v33 op_sel:[1,0] op_sel_hi:[1,1]
	v_pk_mul_f16 v154, v55, v34 op_sel:[1,0] op_sel_hi:[1,1]
	v_pk_mul_f16 v155, v55, v35 op_sel:[1,0] op_sel_hi:[1,1]
	v_mfma_f32_32x32x16_f16 v[0:15], v[144:147], v[116:119], v[0:15]
	v_pk_fma_f16 v152, v47, v36, v152 op_sel:[1,0,0] op_sel_hi:[1,1,1]
	v_pk_fma_f16 v153, v47, v37, v153 op_sel:[1,0,0] op_sel_hi:[1,1,1]
	v_pk_fma_f16 v154, v47, v38, v154 op_sel:[1,0,0] op_sel_hi:[1,1,1]
	v_pk_fma_f16 v155, v47, v39, v155 op_sel:[1,0,0] op_sel_hi:[1,1,1]
	v_mfma_f32_32x32x16_f16 v[16:31], v[148:151], v[120:123], v[16:31]
	v_pk_mul_f16 v156, v55, v36 op_sel:[1,0] op_sel_hi:[1,1]
	v_pk_mul_f16 v157, v55, v37 op_sel:[1,0] op_sel_hi:[1,1]
	v_pk_mul_f16 v158, v55, v38 op_sel:[1,0] op_sel_hi:[1,1]
	v_pk_mul_f16 v159, v55, v39 op_sel:[1,0] op_sel_hi:[1,1]
	v_mfma_f32_32x32x16_f16 v[0:15], v[148:151], v[124:127], v[0:15]
	v_pk_fma_f16 v156, v47, v32, v156 op_sel:[1,0,0] op_sel_hi:[1,1,1] neg_lo:[0,0,1] neg_hi:[0,0,1]
	v_pk_fma_f16 v157, v47, v33, v157 op_sel:[1,0,0] op_sel_hi:[1,1,1] neg_lo:[0,0,1] neg_hi:[0,0,1]
	v_pk_fma_f16 v158, v47, v34, v158 op_sel:[1,0,0] op_sel_hi:[1,1,1] neg_lo:[0,0,1] neg_hi:[0,0,1]
	v_pk_fma_f16 v159, v47, v35, v159 op_sel:[1,0,0] op_sel_hi:[1,1,1] neg_lo:[0,0,1] neg_hi:[0,0,1]
	ds_read_b128 v[80:83], v161
	ds_read_b128 v[84:87], v161 offset:1024
	ds_read_b128 v[88:91], v161 offset:2048
	ds_read_b128 v[92:95], v161 offset:3072
	s_waitcnt lgkmcnt(4)
	v_mfma_f32_32x32x16_f16 v[16:31], v[152:155], v[128:131], v[16:31]
	s_waitcnt vmcnt(6)
	v_pk_mul_f16 v144, v72, v56 op_sel:[0,0] op_sel_hi:[0,1]
	v_pk_mul_f16 v145, v72, v57 op_sel:[0,0] op_sel_hi:[0,1]
	v_pk_mul_f16 v146, v72, v58 op_sel:[0,0] op_sel_hi:[0,1]
	v_pk_mul_f16 v147, v72, v59 op_sel:[0,0] op_sel_hi:[0,1]
	v_mfma_f32_32x32x16_f16 v[0:15], v[152:155], v[132:135], v[0:15]
	v_pk_fma_f16 v144, v64, v60, v144 op_sel:[0,0,0] op_sel_hi:[0,1,1]
	v_pk_fma_f16 v145, v64, v61, v145 op_sel:[0,0,0] op_sel_hi:[0,1,1]
	v_pk_fma_f16 v146, v64, v62, v146 op_sel:[0,0,0] op_sel_hi:[0,1,1]
	v_pk_fma_f16 v147, v64, v63, v147 op_sel:[0,0,0] op_sel_hi:[0,1,1]
	v_mfma_f32_32x32x16_f16 v[16:31], v[156:159], v[136:139], v[16:31]
	v_pk_mul_f16 v148, v72, v60 op_sel:[0,0] op_sel_hi:[0,1]
	v_pk_mul_f16 v149, v72, v61 op_sel:[0,0] op_sel_hi:[0,1]
	v_pk_mul_f16 v150, v72, v62 op_sel:[0,0] op_sel_hi:[0,1]
	v_pk_mul_f16 v151, v72, v63 op_sel:[0,0] op_sel_hi:[0,1]
	v_mfma_f32_32x32x16_f16 v[0:15], v[156:159], v[140:143], v[0:15]
	v_pk_fma_f16 v148, v64, v56, v148 op_sel:[0,0,0] op_sel_hi:[0,1,1] neg_lo:[0,0,1] neg_hi:[0,0,1]
	v_pk_fma_f16 v149, v64, v57, v149 op_sel:[0,0,0] op_sel_hi:[0,1,1] neg_lo:[0,0,1] neg_hi:[0,0,1]
	v_pk_fma_f16 v150, v64, v58, v150 op_sel:[0,0,0] op_sel_hi:[0,1,1] neg_lo:[0,0,1] neg_hi:[0,0,1]
	v_pk_fma_f16 v151, v64, v59, v151 op_sel:[0,0,0] op_sel_hi:[0,1,1] neg_lo:[0,0,1] neg_hi:[0,0,1]
	ds_read_b128 v[96:99], v161 offset:4096
	ds_read_b128 v[100:103], v161 offset:5120
	ds_read_b128 v[104:107], v161 offset:6144
	ds_read_b128 v[108:111], v161 offset:7168
	s_add_u32 s17, s17, 1
	s_cmp_eq_u32 s17, 17
	s_cbranch_scc1 .Lk2_epi

.Lk2_b10:
	s_waitcnt lgkmcnt(4)
	v_mfma_f32_32x32x16_f16 v[16:31], v[144:147], v[80:83], v[16:31]
	s_cmp_le_u32 s22, 16
	s_cselect_b32 s40, s18, 0x1c000
	s_add_u32 m0, s40, s35
	s_add_u32 s22, s22, 1
	global_load_lds_dwordx4 v168, s[20:21]
	global_load_lds_dwordx4 v168, s[20:21] offset:1024
	v_pk_mul_f16 v152, v72, v56 op_sel:[1,0] op_sel_hi:[1,1]
	v_pk_mul_f16 v153, v72, v57 op_sel:[1,0] op_sel_hi:[1,1]
	v_pk_mul_f16 v154, v72, v58 op_sel:[1,0] op_sel_hi:[1,1]
	v_pk_mul_f16 v155, v72, v59 op_sel:[1,0] op_sel_hi:[1,1]
	v_mfma_f32_32x32x16_f16 v[0:15], v[144:147], v[84:87], v[0:15]
	s_cmp_le_u32 s22, 16
	s_cselect_b32 s41, 0x4000, 0
	v_pk_fma_f16 v152, v64, v60, v152 op_sel:[1,0,0] op_sel_hi:[1,1,1]
	v_pk_fma_f16 v153, v64, v61, v153 op_sel:[1,0,0] op_sel_hi:[1,1,1]
	v_pk_fma_f16 v154, v64, v62, v154 op_sel:[1,0,0] op_sel_hi:[1,1,1]
	v_pk_fma_f16 v155, v64, v63, v155 op_sel:[1,0,0] op_sel_hi:[1,1,1]
	v_mfma_f32_32x32x16_f16 v[16:31], v[148:151], v[88:91], v[16:31]
	s_add_u32 s20, s20, s41
	s_addc_u32 s21, s21, 0
	v_pk_mul_f16 v156, v72, v60 op_sel:[1,0] op_sel_hi:[1,1]
	v_pk_mul_f16 v157, v72, v61 op_sel:[1,0] op_sel_hi:[1,1]
	v_pk_mul_f16 v158, v72, v62 op_sel:[1,0] op_sel_hi:[1,1]
	v_pk_mul_f16 v159, v72, v63 op_sel:[1,0] op_sel_hi:[1,1]
	v_mfma_f32_32x32x16_f16 v[0:15], v[148:151], v[92:95], v[0:15]
	s_add_u32 s18, s18, 0x4000
	s_cmp_eq_u32 s18, 0x1c000
	s_cselect_b32 s18, 0, s18
	v_pk_fma_f16 v156, v64, v56, v156 op_sel:[1,0,0] op_sel_hi:[1,1,1] neg_lo:[0,0,1] neg_hi:[0,0,1]
	v_pk_fma_f16 v157, v64, v57, v157 op_sel:[1,0,0] op_sel_hi:[1,1,1] neg_lo:[0,0,1] neg_hi:[0,0,1]
	v_pk_fma_f16 v158, v64, v58, v158 op_sel:[1,0,0] op_sel_hi:[1,1,1] neg_lo:[0,0,1] neg_hi:[0,0,1]
	v_pk_fma_f16 v159, v64, v59, v159 op_sel:[1,0,0] op_sel_hi:[1,1,1] neg_lo:[0,0,1] neg_hi:[0,0,1]
	ds_read_b128 v[112:115], v161 offset:8192
	ds_read_b128 v[116:119], v161 offset:9216
	ds_read_b128 v[120:123], v161 offset:10240
	ds_read_b128 v[124:127], v161 offset:11264
	s_waitcnt lgkmcnt(4)
	v_mfma_f32_32x32x16_f16 v[16:31], v[152:155], v[96:99], v[16:31]
	s_add_u32 s14, s14, 1
	s_cmp_eq_u32 s14, 16
	s_cselect_b32 s42, 1, 0
	v_pk_mul_f16 v144, v73, v56 op_sel:[0,0] op_sel_hi:[0,1]
	v_pk_mul_f16 v145, v73, v57 op_sel:[0,0] op_sel_hi:[0,1]
	v_pk_mul_f16 v146, v73, v58 op_sel:[0,0] op_sel_hi:[0,1]
	v_pk_mul_f16 v147, v73, v59 op_sel:[0,0] op_sel_hi:[0,1]
	v_mfma_f32_32x32x16_f16 v[0:15], v[152:155], v[100:103], v[0:15]
	s_add_u32 s13, s13, s42
	s_cmp_eq_u32 s42, 1
	s_cselect_b32 s14, s13, s14
	v_pk_fma_f16 v144, v65, v60, v144 op_sel:[0,0,0] op_sel_hi:[0,1,1]
	v_pk_fma_f16 v145, v65, v61, v145 op_sel:[0,0,0] op_sel_hi:[0,1,1]
	v_pk_fma_f16 v146, v65, v62, v146 op_sel:[0,0,0] op_sel_hi:[0,1,1]
	v_pk_fma_f16 v147, v65, v63, v147 op_sel:[0,0,0] op_sel_hi:[0,1,1]
	v_mfma_f32_32x32x16_f16 v[16:31], v[156:159], v[104:107], v[16:31]
	s_min_u32 s43, s13, 15
	s_min_u32 s44, s14, 15
	s_lshl_b32 s45, s44, 16
	v_pk_mul_f16 v148, v73, v60 op_sel:[0,0] op_sel_hi:[0,1]
	v_pk_mul_f16 v149, v73, v61 op_sel:[0,0] op_sel_hi:[0,1]
	v_pk_mul_f16 v150, v73, v62 op_sel:[0,0] op_sel_hi:[0,1]
	v_pk_mul_f16 v151, v73, v63 op_sel:[0,0] op_sel_hi:[0,1]
	v_mfma_f32_32x32x16_f16 v[0:15], v[156:159], v[108:111], v[0:15]
	s_add_u32 s24, s8, s45
	s_addc_u32 s25, s9, 0
	v_pk_fma_f16 v148, v65, v56, v148 op_sel:[0,0,0] op_sel_hi:[0,1,1] neg_lo:[0,0,1] neg_hi:[0,0,1]
	v_pk_fma_f16 v149, v65, v57, v149 op_sel:[0,0,0] op_sel_hi:[0,1,1] neg_lo:[0,0,1] neg_hi:[0,0,1]
	v_pk_fma_f16 v150, v65, v58, v150 op_sel:[0,0,0] op_sel_hi:[0,1,1] neg_lo:[0,0,1] neg_hi:[0,0,1]
	v_pk_fma_f16 v151, v65, v59, v151 op_sel:[0,0,0] op_sel_hi:[0,1,1] neg_lo:[0,0,1] neg_hi:[0,0,1]
	ds_read_b128 v[128:131], v161 offset:12288
	ds_read_b128 v[132:135], v161 offset:13312
	ds_read_b128 v[136:139], v161 offset:14336
	ds_read_b128 v[140:143], v161 offset:15360
	s_add_u32 s19, s19, 0x4000
	s_cmp_eq_u32 s19, 0x1c000
	s_cselect_b32 s19, 0, s19
	v_add_u32_e32 v161, s19, v160
	s_waitcnt lgkmcnt(4)
	v_mfma_f32_32x32x16_f16 v[16:31], v[144:147], v[112:115], v[16:31]
	s_add_u32 s26, s24, 0x100000
	s_addc_u32 s27, s25, 0
	s_lshl_b32 s45, s43, 16
	s_add_u32 s28, s8, s45
	s_addc_u32 s29, s9, 0
	v_pk_mul_f16 v152, v73, v56 op_sel:[1,0] op_sel_hi:[1,1]
	v_pk_mul_f16 v153, v73, v57 op_sel:[1,0] op_sel_hi:[1,1]
	v_pk_mul_f16 v154, v73, v58 op_sel:[1,0] op_sel_hi:[1,1]
	v_pk_mul_f16 v155, v73, v59 op_sel:[1,0] op_sel_hi:[1,1]
	v_mfma_f32_32x32x16_f16 v[0:15], v[144:147], v[116:119], v[0:15]
	s_add_u32 s30, s28, 0x100000
	s_addc_u32 s31, s29, 0
	v_pk_fma_f16 v152, v65, v60, v152 op_sel:[1,0,0] op_sel_hi:[1,1,1]
	v_pk_fma_f16 v153, v65, v61, v153 op_sel:[1,0,0] op_sel_hi:[1,1,1]
	v_pk_fma_f16 v154, v65, v62, v154 op_sel:[1,0,0] op_sel_hi:[1,1,1]
	v_pk_fma_f16 v155, v65, v63, v155 op_sel:[1,0,0] op_sel_hi:[1,1,1]
	v_mfma_f32_32x32x16_f16 v[16:31], v[148:151], v[120:123], v[16:31]
	global_load_dwordx4 v[36:39], v164, s[24:25]
	v_pk_mul_f16 v156, v73, v60 op_sel:[1,0] op_sel_hi:[1,1]
	v_pk_mul_f16 v157, v73, v61 op_sel:[1,0] op_sel_hi:[1,1]
	v_pk_mul_f16 v158, v73, v62 op_sel:[1,0] op_sel_hi:[1,1]
	v_pk_mul_f16 v159, v73, v63 op_sel:[1,0] op_sel_hi:[1,1]
	v_mfma_f32_32x32x16_f16 v[0:15], v[148:151], v[124:127], v[0:15]
	global_load_dwordx4 v[32:35], v164, s[26:27]
	v_pk_fma_f16 v156, v65, v56, v156 op_sel:[1,0,0] op_sel_hi:[1,1,1] neg_lo:[0,0,1] neg_hi:[0,0,1]
	v_pk_fma_f16 v157, v65, v57, v157 op_sel:[1,0,0] op_sel_hi:[1,1,1] neg_lo:[0,0,1] neg_hi:[0,0,1]
	v_pk_fma_f16 v158, v65, v58, v158 op_sel:[1,0,0] op_sel_hi:[1,1,1] neg_lo:[0,0,1] neg_hi:[0,0,1]
	v_pk_fma_f16 v159, v65, v59, v159 op_sel:[1,0,0] op_sel_hi:[1,1,1] neg_lo:[0,0,1] neg_hi:[0,0,1]
	ds_read_b128 v[80:83], v161
	ds_read_b128 v[84:87], v161 offset:1024
	ds_read_b128 v[88:91], v161 offset:2048
	ds_read_b128 v[92:95], v161 offset:3072
	s_waitcnt lgkmcnt(4)
	v_mfma_f32_32x32x16_f16 v[16:31], v[152:155], v[128:131], v[16:31]
	global_load_dwordx4 v[40:43], v165, s[28:29]
	v_pk_mul_f16 v144, v74, v56 op_sel:[0,0] op_sel_hi:[0,1]
	v_pk_mul_f16 v145, v74, v57 op_sel:[0,0] op_sel_hi:[0,1]
	v_pk_mul_f16 v146, v74, v58 op_sel:[0,0] op_sel_hi:[0,1]
	v_pk_mul_f16 v147, v74, v59 op_sel:[0,0] op_sel_hi:[0,1]
	v_mfma_f32_32x32x16_f16 v[0:15], v[152:155], v[132:135], v[0:15]
	global_load_dwordx4 v[44:47], v166, s[28:29]
	v_pk_fma_f16 v144, v66, v60, v144 op_sel:[0,0,0] op_sel_hi:[0,1,1]
	v_pk_fma_f16 v145, v66, v61, v145 op_sel:[0,0,0] op_sel_hi:[0,1,1]
	v_pk_fma_f16 v146, v66, v62, v146 op_sel:[0,0,0] op_sel_hi:[0,1,1]
	v_pk_fma_f16 v147, v66, v63, v147 op_sel:[0,0,0] op_sel_hi:[0,1,1]
	v_mfma_f32_32x32x16_f16 v[16:31], v[156:159], v[136:139], v[16:31]
	global_load_dwordx4 v[48:51], v165, s[30:31]
	v_pk_mul_f16 v148, v74, v60 op_sel:[0,0] op_sel_hi:[0,1]
	v_pk_mul_f16 v149, v74, v61 op_sel:[0,0] op_sel_hi:[0,1]
	v_pk_mul_f16 v150, v74, v62 op_sel:[0,0] op_sel_hi:[0,1]
	v_pk_mul_f16 v151, v74, v63 op_sel:[0,0] op_sel_hi:[0,1]
	v_mfma_f32_32x32x16_f16 v[0:15], v[156:159], v[140:143], v[0:15]
	global_load_dwordx4 v[52:55], v166, s[30:31]
	v_pk_fma_f16 v148, v66, v56, v148 op_sel:[0,0,0] op_sel_hi:[0,1,1] neg_lo:[0,0,1] neg_hi:[0,0,1]
	v_pk_fma_f16 v149, v66, v57, v149 op_sel:[0,0,0] op_sel_hi:[0,1,1] neg_lo:[0,0,1] neg_hi:[0,0,1]
	v_pk_fma_f16 v150, v66, v58, v150 op_sel:[0,0,0] op_sel_hi:[0,1,1] neg_lo:[0,0,1] neg_hi:[0,0,1]
	v_pk_fma_f16 v151, v66, v59, v151 op_sel:[0,0,0] op_sel_hi:[0,1,1] neg_lo:[0,0,1] neg_hi:[0,0,1]
	ds_read_b128 v[96:99], v161 offset:4096
	ds_read_b128 v[100:103], v161 offset:5120
	ds_read_b128 v[104:107], v161 offset:6144
	ds_read_b128 v[108:111], v161 offset:7168
	s_add_u32 s17, s17, 1
	s_cmp_eq_u32 s17, 17
	s_cbranch_scc1 .Lk2_epi

.Lk2_b11:
	s_waitcnt lgkmcnt(4)
	v_mfma_f32_32x32x16_f16 v[16:31], v[144:147], v[80:83], v[16:31]
	s_cmp_le_u32 s22, 16
	s_cselect_b32 s40, s18, 0x1c000
	s_add_u32 m0, s40, s35
	v_pk_mul_f16 v152, v74, v56 op_sel:[1,0] op_sel_hi:[1,1]
	v_pk_mul_f16 v153, v74, v57 op_sel:[1,0] op_sel_hi:[1,1]
	v_pk_mul_f16 v154, v74, v58 op_sel:[1,0] op_sel_hi:[1,1]
	v_pk_mul_f16 v155, v74, v59 op_sel:[1,0] op_sel_hi:[1,1]
	v_mfma_f32_32x32x16_f16 v[0:15], v[144:147], v[84:87], v[0:15]
	s_add_u32 s22, s22, 1
	global_load_lds_dwordx4 v168, s[20:21]
	global_load_lds_dwordx4 v168, s[20:21] offset:1024
	v_pk_fma_f16 v152, v66, v60, v152 op_sel:[1,0,0] op_sel_hi:[1,1,1]
	v_pk_fma_f16 v153, v66, v61, v153 op_sel:[1,0,0] op_sel_hi:[1,1,1]
	v_pk_fma_f16 v154, v66, v62, v154 op_sel:[1,0,0] op_sel_hi:[1,1,1]
	v_pk_fma_f16 v155, v66, v63, v155 op_sel:[1,0,0] op_sel_hi:[1,1,1]
	v_mfma_f32_32x32x16_f16 v[16:31], v[148:151], v[88:91], v[16:31]
	s_cmp_le_u32 s22, 16
	s_cselect_b32 s41, 0x4000, 0
	v_pk_mul_f16 v156, v74, v60 op_sel:[1,0] op_sel_hi:[1,1]
	v_pk_mul_f16 v157, v74, v61 op_sel:[1,0] op_sel_hi:[1,1]
	v_pk_mul_f16 v158, v74, v62 op_sel:[1,0] op_sel_hi:[1,1]
	v_pk_mul_f16 v159, v74, v63 op_sel:[1,0] op_sel_hi:[1,1]
	v_mfma_f32_32x32x16_f16 v[0:15], v[148:151], v[92:95], v[0:15]
	s_add_u32 s20, s20, s41
	s_addc_u32 s21, s21, 0
	v_pk_fma_f16 v156, v66, v56, v156 op_sel:[1,0,0] op_sel_hi:[1,1,1] neg_lo:[0,0,1] neg_hi:[0,0,1]
	v_pk_fma_f16 v157, v66, v57, v157 op_sel:[1,0,0] op_sel_hi:[1,1,1] neg_lo:[0,0,1] neg_hi:[0,0,1]
	v_pk_fma_f16 v158, v66, v58, v158 op_sel:[1,0,0] op_sel_hi:[1,1,1] neg_lo:[0,0,1] neg_hi:[0,0,1]
	v_pk_fma_f16 v159, v66, v59, v159 op_sel:[1,0,0] op_sel_hi:[1,1,1] neg_lo:[0,0,1] neg_hi:[0,0,1]
	ds_read_b128 v[112:115], v161 offset:8192
	ds_read_b128 v[116:119], v161 offset:9216
	ds_read_b128 v[120:123], v161 offset:10240
	ds_read_b128 v[124:127], v161 offset:11264
	s_waitcnt lgkmcnt(4)
	v_mfma_f32_32x32x16_f16 v[16:31], v[152:155], v[96:99], v[16:31]
	s_add_u32 s18, s18, 0x4000
	s_cmp_eq_u32 s18, 0x1c000
	s_cselect_b32 s18, 0, s18
	v_pk_mul_f16 v144, v75, v56 op_sel:[0,0] op_sel_hi:[0,1]
	v_pk_mul_f16 v145, v75, v57 op_sel:[0,0] op_sel_hi:[0,1]
	v_pk_mul_f16 v146, v75, v58 op_sel:[0,0] op_sel_hi:[0,1]
	v_pk_mul_f16 v147, v75, v59 op_sel:[0,0] op_sel_hi:[0,1]
	v_mfma_f32_32x32x16_f16 v[0:15], v[152:155], v[100:103], v[0:15]
	v_pk_fma_f16 v144, v67, v60, v144 op_sel:[0,0,0] op_sel_hi:[0,1,1]
	v_pk_fma_f16 v145, v67, v61, v145 op_sel:[0,0,0] op_sel_hi:[0,1,1]
	v_pk_fma_f16 v146, v67, v62, v146 op_sel:[0,0,0] op_sel_hi:[0,1,1]
	v_pk_fma_f16 v147, v67, v63, v147 op_sel:[0,0,0] op_sel_hi:[0,1,1]
	v_mfma_f32_32x32x16_f16 v[16:31], v[156:159], v[104:107], v[16:31]
	v_pk_mul_f16 v148, v75, v60 op_sel:[0,0] op_sel_hi:[0,1]
	v_pk_mul_f16 v149, v75, v61 op_sel:[0,0] op_sel_hi:[0,1]
	v_pk_mul_f16 v150, v75, v62 op_sel:[0,0] op_sel_hi:[0,1]
	v_pk_mul_f16 v151, v75, v63 op_sel:[0,0] op_sel_hi:[0,1]
	v_mfma_f32_32x32x16_f16 v[0:15], v[156:159], v[108:111], v[0:15]
	v_pk_fma_f16 v148, v67, v56, v148 op_sel:[0,0,0] op_sel_hi:[0,1,1] neg_lo:[0,0,1] neg_hi:[0,0,1]
	v_pk_fma_f16 v149, v67, v57, v149 op_sel:[0,0,0] op_sel_hi:[0,1,1] neg_lo:[0,0,1] neg_hi:[0,0,1]
	v_pk_fma_f16 v150, v67, v58, v150 op_sel:[0,0,0] op_sel_hi:[0,1,1] neg_lo:[0,0,1] neg_hi:[0,0,1]
	v_pk_fma_f16 v151, v67, v59, v151 op_sel:[0,0,0] op_sel_hi:[0,1,1] neg_lo:[0,0,1] neg_hi:[0,0,1]
	ds_read_b128 v[128:131], v161 offset:12288
	ds_read_b128 v[132:135], v161 offset:13312
	ds_read_b128 v[136:139], v161 offset:14336
	ds_read_b128 v[140:143], v161 offset:15360
	s_add_u32 s19, s19, 0x4000
	s_cmp_eq_u32 s19, 0x1c000
	s_cselect_b32 s19, 0, s19
	v_add_u32_e32 v161, s19, v160
	s_waitcnt lgkmcnt(4)
	v_mfma_f32_32x32x16_f16 v[16:31], v[144:147], v[112:115], v[16:31]
	v_pk_mul_f16 v152, v75, v56 op_sel:[1,0] op_sel_hi:[1,1]
	v_pk_mul_f16 v153, v75, v57 op_sel:[1,0] op_sel_hi:[1,1]
	v_pk_mul_f16 v154, v75, v58 op_sel:[1,0] op_sel_hi:[1,1]
	v_pk_mul_f16 v155, v75, v59 op_sel:[1,0] op_sel_hi:[1,1]
	v_mfma_f32_32x32x16_f16 v[0:15], v[144:147], v[116:119], v[0:15]
	v_pk_fma_f16 v152, v67, v60, v152 op_sel:[1,0,0] op_sel_hi:[1,1,1]
	v_pk_fma_f16 v153, v67, v61, v153 op_sel:[1,0,0] op_sel_hi:[1,1,1]
	v_pk_fma_f16 v154, v67, v62, v154 op_sel:[1,0,0] op_sel_hi:[1,1,1]
	v_pk_fma_f16 v155, v67, v63, v155 op_sel:[1,0,0] op_sel_hi:[1,1,1]
	v_mfma_f32_32x32x16_f16 v[16:31], v[148:151], v[120:123], v[16:31]
	v_pk_mul_f16 v156, v75, v60 op_sel:[1,0] op_sel_hi:[1,1]
	v_pk_mul_f16 v157, v75, v61 op_sel:[1,0] op_sel_hi:[1,1]
	v_pk_mul_f16 v158, v75, v62 op_sel:[1,0] op_sel_hi:[1,1]
	v_pk_mul_f16 v159, v75, v63 op_sel:[1,0] op_sel_hi:[1,1]
	v_mfma_f32_32x32x16_f16 v[0:15], v[148:151], v[124:127], v[0:15]
	v_pk_fma_f16 v156, v67, v56, v156 op_sel:[1,0,0] op_sel_hi:[1,1,1] neg_lo:[0,0,1] neg_hi:[0,0,1]
	v_pk_fma_f16 v157, v67, v57, v157 op_sel:[1,0,0] op_sel_hi:[1,1,1] neg_lo:[0,0,1] neg_hi:[0,0,1]
	v_pk_fma_f16 v158, v67, v58, v158 op_sel:[1,0,0] op_sel_hi:[1,1,1] neg_lo:[0,0,1] neg_hi:[0,0,1]
	v_pk_fma_f16 v159, v67, v59, v159 op_sel:[1,0,0] op_sel_hi:[1,1,1] neg_lo:[0,0,1] neg_hi:[0,0,1]
	ds_read_b128 v[80:83], v161
	ds_read_b128 v[84:87], v161 offset:1024
	ds_read_b128 v[88:91], v161 offset:2048
	ds_read_b128 v[92:95], v161 offset:3072
	s_waitcnt lgkmcnt(4)
	v_mfma_f32_32x32x16_f16 v[16:31], v[152:155], v[128:131], v[16:31]
	v_pk_mul_f16 v144, v76, v56 op_sel:[0,0] op_sel_hi:[0,1]
	v_pk_mul_f16 v145, v76, v57 op_sel:[0,0] op_sel_hi:[0,1]
	v_pk_mul_f16 v146, v76, v58 op_sel:[0,0] op_sel_hi:[0,1]
	v_pk_mul_f16 v147, v76, v59 op_sel:[0,0] op_sel_hi:[0,1]
	v_mfma_f32_32x32x16_f16 v[0:15], v[152:155], v[132:135], v[0:15]
	v_pk_fma_f16 v144, v68, v60, v144 op_sel:[0,0,0] op_sel_hi:[0,1,1]
	v_pk_fma_f16 v145, v68, v61, v145 op_sel:[0,0,0] op_sel_hi:[0,1,1]
	v_pk_fma_f16 v146, v68, v62, v146 op_sel:[0,0,0] op_sel_hi:[0,1,1]
	v_pk_fma_f16 v147, v68, v63, v147 op_sel:[0,0,0] op_sel_hi:[0,1,1]
	v_mfma_f32_32x32x16_f16 v[16:31], v[156:159], v[136:139], v[16:31]
	v_pk_mul_f16 v148, v76, v60 op_sel:[0,0] op_sel_hi:[0,1]
	v_pk_mul_f16 v149, v76, v61 op_sel:[0,0] op_sel_hi:[0,1]
	v_pk_mul_f16 v150, v76, v62 op_sel:[0,0] op_sel_hi:[0,1]
	v_pk_mul_f16 v151, v76, v63 op_sel:[0,0] op_sel_hi:[0,1]
	v_mfma_f32_32x32x16_f16 v[0:15], v[156:159], v[140:143], v[0:15]
	v_pk_fma_f16 v148, v68, v56, v148 op_sel:[0,0,0] op_sel_hi:[0,1,1] neg_lo:[0,0,1] neg_hi:[0,0,1]
	v_pk_fma_f16 v149, v68, v57, v149 op_sel:[0,0,0] op_sel_hi:[0,1,1] neg_lo:[0,0,1] neg_hi:[0,0,1]
	v_pk_fma_f16 v150, v68, v58, v150 op_sel:[0,0,0] op_sel_hi:[0,1,1] neg_lo:[0,0,1] neg_hi:[0,0,1]
	v_pk_fma_f16 v151, v68, v59, v151 op_sel:[0,0,0] op_sel_hi:[0,1,1] neg_lo:[0,0,1] neg_hi:[0,0,1]
	ds_read_b128 v[96:99], v161 offset:4096
	ds_read_b128 v[100:103], v161 offset:5120
	ds_read_b128 v[104:107], v161 offset:6144
	ds_read_b128 v[108:111], v161 offset:7168
	s_add_u32 s17, s17, 1
	s_cmp_eq_u32 s17, 17
	s_cbranch_scc1 .Lk2_epi

.Lk2_b12:
	s_waitcnt lgkmcnt(4)
	v_mfma_f32_32x32x16_f16 v[16:31], v[144:147], v[80:83], v[16:31]
	s_cmp_le_u32 s22, 16
	s_cselect_b32 s40, s18, 0x1c000
	s_add_u32 m0, s40, s35
	v_pk_mul_f16 v152, v76, v56 op_sel:[1,0] op_sel_hi:[1,1]
	v_pk_mul_f16 v153, v76, v57 op_sel:[1,0] op_sel_hi:[1,1]
	v_pk_mul_f16 v154, v76, v58 op_sel:[1,0] op_sel_hi:[1,1]
	v_pk_mul_f16 v155, v76, v59 op_sel:[1,0] op_sel_hi:[1,1]
	v_mfma_f32_32x32x16_f16 v[0:15], v[144:147], v[84:87], v[0:15]
	s_add_u32 s22, s22, 1
	global_load_lds_dwordx4 v168, s[20:21]
	global_load_lds_dwordx4 v168, s[20:21] offset:1024
	v_pk_fma_f16 v152, v68, v60, v152 op_sel:[1,0,0] op_sel_hi:[1,1,1]
	v_pk_fma_f16 v153, v68, v61, v153 op_sel:[1,0,0] op_sel_hi:[1,1,1]
	v_pk_fma_f16 v154, v68, v62, v154 op_sel:[1,0,0] op_sel_hi:[1,1,1]
	v_pk_fma_f16 v155, v68, v63, v155 op_sel:[1,0,0] op_sel_hi:[1,1,1]
	v_mfma_f32_32x32x16_f16 v[16:31], v[148:151], v[88:91], v[16:31]
	s_cmp_le_u32 s22, 16
	s_cselect_b32 s41, 0x4000, 0
	v_pk_mul_f16 v156, v76, v60 op_sel:[1,0] op_sel_hi:[1,1]
	v_pk_mul_f16 v157, v76, v61 op_sel:[1,0] op_sel_hi:[1,1]
	v_pk_mul_f16 v158, v76, v62 op_sel:[1,0] op_sel_hi:[1,1]
	v_pk_mul_f16 v159, v76, v63 op_sel:[1,0] op_sel_hi:[1,1]
	v_mfma_f32_32x32x16_f16 v[0:15], v[148:151], v[92:95], v[0:15]
	s_add_u32 s20, s20, s41
	s_addc_u32 s21, s21, 0
	v_pk_fma_f16 v156, v68, v56, v156 op_sel:[1,0,0] op_sel_hi:[1,1,1] neg_lo:[0,0,1] neg_hi:[0,0,1]
	v_pk_fma_f16 v157, v68, v57, v157 op_sel:[1,0,0] op_sel_hi:[1,1,1] neg_lo:[0,0,1] neg_hi:[0,0,1]
	v_pk_fma_f16 v158, v68, v58, v158 op_sel:[1,0,0] op_sel_hi:[1,1,1] neg_lo:[0,0,1] neg_hi:[0,0,1]
	v_pk_fma_f16 v159, v68, v59, v159 op_sel:[1,0,0] op_sel_hi:[1,1,1] neg_lo:[0,0,1] neg_hi:[0,0,1]
	ds_read_b128 v[112:115], v161 offset:8192
	ds_read_b128 v[116:119], v161 offset:9216
	ds_read_b128 v[120:123], v161 offset:10240
	ds_read_b128 v[124:127], v161 offset:11264
	s_waitcnt lgkmcnt(4)
	v_mfma_f32_32x32x16_f16 v[16:31], v[152:155], v[96:99], v[16:31]
	s_add_u32 s18, s18, 0x4000
	s_cmp_eq_u32 s18, 0x1c000
	s_cselect_b32 s18, 0, s18
	v_pk_mul_f16 v144, v77, v56 op_sel:[0,0] op_sel_hi:[0,1]
	v_pk_mul_f16 v145, v77, v57 op_sel:[0,0] op_sel_hi:[0,1]
	v_pk_mul_f16 v146, v77, v58 op_sel:[0,0] op_sel_hi:[0,1]
	v_pk_mul_f16 v147, v77, v59 op_sel:[0,0] op_sel_hi:[0,1]
	v_mfma_f32_32x32x16_f16 v[0:15], v[152:155], v[100:103], v[0:15]
	v_pk_fma_f16 v144, v69, v60, v144 op_sel:[0,0,0] op_sel_hi:[0,1,1]
	v_pk_fma_f16 v145, v69, v61, v145 op_sel:[0,0,0] op_sel_hi:[0,1,1]
	v_pk_fma_f16 v146, v69, v62, v146 op_sel:[0,0,0] op_sel_hi:[0,1,1]
	v_pk_fma_f16 v147, v69, v63, v147 op_sel:[0,0,0] op_sel_hi:[0,1,1]
	v_mfma_f32_32x32x16_f16 v[16:31], v[156:159], v[104:107], v[16:31]
	v_pk_mul_f16 v148, v77, v60 op_sel:[0,0] op_sel_hi:[0,1]
	v_pk_mul_f16 v149, v77, v61 op_sel:[0,0] op_sel_hi:[0,1]
	v_pk_mul_f16 v150, v77, v62 op_sel:[0,0] op_sel_hi:[0,1]
	v_pk_mul_f16 v151, v77, v63 op_sel:[0,0] op_sel_hi:[0,1]
	v_mfma_f32_32x32x16_f16 v[0:15], v[156:159], v[108:111], v[0:15]
	v_pk_fma_f16 v148, v69, v56, v148 op_sel:[0,0,0] op_sel_hi:[0,1,1] neg_lo:[0,0,1] neg_hi:[0,0,1]
	v_pk_fma_f16 v149, v69, v57, v149 op_sel:[0,0,0] op_sel_hi:[0,1,1] neg_lo:[0,0,1] neg_hi:[0,0,1]
	v_pk_fma_f16 v150, v69, v58, v150 op_sel:[0,0,0] op_sel_hi:[0,1,1] neg_lo:[0,0,1] neg_hi:[0,0,1]
	v_pk_fma_f16 v151, v69, v59, v151 op_sel:[0,0,0] op_sel_hi:[0,1,1] neg_lo:[0,0,1] neg_hi:[0,0,1]
	ds_read_b128 v[128:131], v161 offset:12288
	ds_read_b128 v[132:135], v161 offset:13312
	ds_read_b128 v[136:139], v161 offset:14336
	ds_read_b128 v[140:143], v161 offset:15360
	s_add_u32 s19, s19, 0x4000
	s_cmp_eq_u32 s19, 0x1c000
	s_cselect_b32 s19, 0, s19
	v_add_u32_e32 v161, s19, v160
	s_waitcnt lgkmcnt(4)
	v_mfma_f32_32x32x16_f16 v[16:31], v[144:147], v[112:115], v[16:31]
	v_pk_mul_f16 v152, v77, v56 op_sel:[1,0] op_sel_hi:[1,1]
	v_pk_mul_f16 v153, v77, v57 op_sel:[1,0] op_sel_hi:[1,1]
	v_pk_mul_f16 v154, v77, v58 op_sel:[1,0] op_sel_hi:[1,1]
	v_pk_mul_f16 v155, v77, v59 op_sel:[1,0] op_sel_hi:[1,1]
	v_mfma_f32_32x32x16_f16 v[0:15], v[144:147], v[116:119], v[0:15]
	v_pk_fma_f16 v152, v69, v60, v152 op_sel:[1,0,0] op_sel_hi:[1,1,1]
	v_pk_fma_f16 v153, v69, v61, v153 op_sel:[1,0,0] op_sel_hi:[1,1,1]
	v_pk_fma_f16 v154, v69, v62, v154 op_sel:[1,0,0] op_sel_hi:[1,1,1]
	v_pk_fma_f16 v155, v69, v63, v155 op_sel:[1,0,0] op_sel_hi:[1,1,1]
	v_mfma_f32_32x32x16_f16 v[16:31], v[148:151], v[120:123], v[16:31]
	v_pk_mul_f16 v156, v77, v60 op_sel:[1,0] op_sel_hi:[1,1]
	v_pk_mul_f16 v157, v77, v61 op_sel:[1,0] op_sel_hi:[1,1]
	v_pk_mul_f16 v158, v77, v62 op_sel:[1,0] op_sel_hi:[1,1]
	v_pk_mul_f16 v159, v77, v63 op_sel:[1,0] op_sel_hi:[1,1]
	v_mfma_f32_32x32x16_f16 v[0:15], v[148:151], v[124:127], v[0:15]
	v_pk_fma_f16 v156, v69, v56, v156 op_sel:[1,0,0] op_sel_hi:[1,1,1] neg_lo:[0,0,1] neg_hi:[0,0,1]
	v_pk_fma_f16 v157, v69, v57, v157 op_sel:[1,0,0] op_sel_hi:[1,1,1] neg_lo:[0,0,1] neg_hi:[0,0,1]
	v_pk_fma_f16 v158, v69, v58, v158 op_sel:[1,0,0] op_sel_hi:[1,1,1] neg_lo:[0,0,1] neg_hi:[0,0,1]
	v_pk_fma_f16 v159, v69, v59, v159 op_sel:[1,0,0] op_sel_hi:[1,1,1] neg_lo:[0,0,1] neg_hi:[0,0,1]
	ds_read_b128 v[80:83], v161
	ds_read_b128 v[84:87], v161 offset:1024
	ds_read_b128 v[88:91], v161 offset:2048
	ds_read_b128 v[92:95], v161 offset:3072
	s_waitcnt lgkmcnt(4)
	v_mfma_f32_32x32x16_f16 v[16:31], v[152:155], v[128:131], v[16:31]
	v_pk_mul_f16 v144, v78, v56 op_sel:[0,0] op_sel_hi:[0,1]
	v_pk_mul_f16 v145, v78, v57 op_sel:[0,0] op_sel_hi:[0,1]
	v_pk_mul_f16 v146, v78, v58 op_sel:[0,0] op_sel_hi:[0,1]
	v_pk_mul_f16 v147, v78, v59 op_sel:[0,0] op_sel_hi:[0,1]
	v_mfma_f32_32x32x16_f16 v[0:15], v[152:155], v[132:135], v[0:15]
	v_pk_fma_f16 v144, v70, v60, v144 op_sel:[0,0,0] op_sel_hi:[0,1,1]
	v_pk_fma_f16 v145, v70, v61, v145 op_sel:[0,0,0] op_sel_hi:[0,1,1]
	v_pk_fma_f16 v146, v70, v62, v146 op_sel:[0,0,0] op_sel_hi:[0,1,1]
	v_pk_fma_f16 v147, v70, v63, v147 op_sel:[0,0,0] op_sel_hi:[0,1,1]
	v_mfma_f32_32x32x16_f16 v[16:31], v[156:159], v[136:139], v[16:31]
	v_pk_mul_f16 v148, v78, v60 op_sel:[0,0] op_sel_hi:[0,1]
	v_pk_mul_f16 v149, v78, v61 op_sel:[0,0] op_sel_hi:[0,1]
	v_pk_mul_f16 v150, v78, v62 op_sel:[0,0] op_sel_hi:[0,1]
	v_pk_mul_f16 v151, v78, v63 op_sel:[0,0] op_sel_hi:[0,1]
	v_mfma_f32_32x32x16_f16 v[0:15], v[156:159], v[140:143], v[0:15]
	v_pk_fma_f16 v148, v70, v56, v148 op_sel:[0,0,0] op_sel_hi:[0,1,1] neg_lo:[0,0,1] neg_hi:[0,0,1]
	v_pk_fma_f16 v149, v70, v57, v149 op_sel:[0,0,0] op_sel_hi:[0,1,1] neg_lo:[0,0,1] neg_hi:[0,0,1]
	v_pk_fma_f16 v150, v70, v58, v150 op_sel:[0,0,0] op_sel_hi:[0,1,1] neg_lo:[0,0,1] neg_hi:[0,0,1]
	v_pk_fma_f16 v151, v70, v59, v151 op_sel:[0,0,0] op_sel_hi:[0,1,1] neg_lo:[0,0,1] neg_hi:[0,0,1]
	ds_read_b128 v[96:99], v161 offset:4096
	ds_read_b128 v[100:103], v161 offset:5120
	ds_read_b128 v[104:107], v161 offset:6144
	ds_read_b128 v[108:111], v161 offset:7168
	s_add_u32 s17, s17, 1
	s_cmp_eq_u32 s17, 17
	s_cbranch_scc1 .Lk2_epi

.Lk2_b13:
	s_waitcnt lgkmcnt(4)
	v_mfma_f32_32x32x16_f16 v[16:31], v[144:147], v[80:83], v[16:31]
	s_cmp_le_u32 s22, 16
	s_cselect_b32 s40, s18, 0x1c000
	s_add_u32 m0, s40, s35
	v_pk_mul_f16 v152, v78, v56 op_sel:[1,0] op_sel_hi:[1,1]
	v_pk_mul_f16 v153, v78, v57 op_sel:[1,0] op_sel_hi:[1,1]
	v_pk_mul_f16 v154, v78, v58 op_sel:[1,0] op_sel_hi:[1,1]
	v_pk_mul_f16 v155, v78, v59 op_sel:[1,0] op_sel_hi:[1,1]
	v_mfma_f32_32x32x16_f16 v[0:15], v[144:147], v[84:87], v[0:15]
	s_add_u32 s22, s22, 1
	global_load_lds_dwordx4 v168, s[20:21]
	global_load_lds_dwordx4 v168, s[20:21] offset:1024
	v_pk_fma_f16 v152, v70, v60, v152 op_sel:[1,0,0] op_sel_hi:[1,1,1]
	v_pk_fma_f16 v153, v70, v61, v153 op_sel:[1,0,0] op_sel_hi:[1,1,1]
	v_pk_fma_f16 v154, v70, v62, v154 op_sel:[1,0,0] op_sel_hi:[1,1,1]
	v_pk_fma_f16 v155, v70, v63, v155 op_sel:[1,0,0] op_sel_hi:[1,1,1]
	v_mfma_f32_32x32x16_f16 v[16:31], v[148:151], v[88:91], v[16:31]
	s_cmp_le_u32 s22, 16
	s_cselect_b32 s41, 0x4000, 0
	v_pk_mul_f16 v156, v78, v60 op_sel:[1,0] op_sel_hi:[1,1]
	v_pk_mul_f16 v157, v78, v61 op_sel:[1,0] op_sel_hi:[1,1]
	v_pk_mul_f16 v158, v78, v62 op_sel:[1,0] op_sel_hi:[1,1]
	v_pk_mul_f16 v159, v78, v63 op_sel:[1,0] op_sel_hi:[1,1]
	v_mfma_f32_32x32x16_f16 v[0:15], v[148:151], v[92:95], v[0:15]
	s_add_u32 s20, s20, s41
	s_addc_u32 s21, s21, 0
	v_pk_fma_f16 v156, v70, v56, v156 op_sel:[1,0,0] op_sel_hi:[1,1,1] neg_lo:[0,0,1] neg_hi:[0,0,1]
	v_pk_fma_f16 v157, v70, v57, v157 op_sel:[1,0,0] op_sel_hi:[1,1,1] neg_lo:[0,0,1] neg_hi:[0,0,1]
	v_pk_fma_f16 v158, v70, v58, v158 op_sel:[1,0,0] op_sel_hi:[1,1,1] neg_lo:[0,0,1] neg_hi:[0,0,1]
	v_pk_fma_f16 v159, v70, v59, v159 op_sel:[1,0,0] op_sel_hi:[1,1,1] neg_lo:[0,0,1] neg_hi:[0,0,1]
	ds_read_b128 v[112:115], v161 offset:8192
	ds_read_b128 v[116:119], v161 offset:9216
	ds_read_b128 v[120:123], v161 offset:10240
	ds_read_b128 v[124:127], v161 offset:11264
	s_waitcnt lgkmcnt(4)
	v_mfma_f32_32x32x16_f16 v[16:31], v[152:155], v[96:99], v[16:31]
	s_add_u32 s18, s18, 0x4000
	s_cmp_eq_u32 s18, 0x1c000
	s_cselect_b32 s18, 0, s18
	v_pk_mul_f16 v144, v79, v56 op_sel:[0,0] op_sel_hi:[0,1]
	v_pk_mul_f16 v145, v79, v57 op_sel:[0,0] op_sel_hi:[0,1]
	v_pk_mul_f16 v146, v79, v58 op_sel:[0,0] op_sel_hi:[0,1]
	v_pk_mul_f16 v147, v79, v59 op_sel:[0,0] op_sel_hi:[0,1]
	v_mfma_f32_32x32x16_f16 v[0:15], v[152:155], v[100:103], v[0:15]
	v_pk_fma_f16 v144, v71, v60, v144 op_sel:[0,0,0] op_sel_hi:[0,1,1]
	v_pk_fma_f16 v145, v71, v61, v145 op_sel:[0,0,0] op_sel_hi:[0,1,1]
	v_pk_fma_f16 v146, v71, v62, v146 op_sel:[0,0,0] op_sel_hi:[0,1,1]
	v_pk_fma_f16 v147, v71, v63, v147 op_sel:[0,0,0] op_sel_hi:[0,1,1]
	v_mfma_f32_32x32x16_f16 v[16:31], v[156:159], v[104:107], v[16:31]
	v_pk_mul_f16 v148, v79, v60 op_sel:[0,0] op_sel_hi:[0,1]
	v_pk_mul_f16 v149, v79, v61 op_sel:[0,0] op_sel_hi:[0,1]
	v_pk_mul_f16 v150, v79, v62 op_sel:[0,0] op_sel_hi:[0,1]
	v_pk_mul_f16 v151, v79, v63 op_sel:[0,0] op_sel_hi:[0,1]
	v_mfma_f32_32x32x16_f16 v[0:15], v[156:159], v[108:111], v[0:15]
	v_pk_fma_f16 v148, v71, v56, v148 op_sel:[0,0,0] op_sel_hi:[0,1,1] neg_lo:[0,0,1] neg_hi:[0,0,1]
	v_pk_fma_f16 v149, v71, v57, v149 op_sel:[0,0,0] op_sel_hi:[0,1,1] neg_lo:[0,0,1] neg_hi:[0,0,1]
	v_pk_fma_f16 v150, v71, v58, v150 op_sel:[0,0,0] op_sel_hi:[0,1,1] neg_lo:[0,0,1] neg_hi:[0,0,1]
	v_pk_fma_f16 v151, v71, v59, v151 op_sel:[0,0,0] op_sel_hi:[0,1,1] neg_lo:[0,0,1] neg_hi:[0,0,1]
	ds_read_b128 v[128:131], v161 offset:12288
	ds_read_b128 v[132:135], v161 offset:13312
	ds_read_b128 v[136:139], v161 offset:14336
	ds_read_b128 v[140:143], v161 offset:15360
	s_add_u32 s19, s19, 0x4000
	s_cmp_eq_u32 s19, 0x1c000
	s_cselect_b32 s19, 0, s19
	v_add_u32_e32 v161, s19, v160
	s_waitcnt lgkmcnt(4)
	v_mfma_f32_32x32x16_f16 v[16:31], v[144:147], v[112:115], v[16:31]
	v_pk_mul_f16 v152, v79, v56 op_sel:[1,0] op_sel_hi:[1,1]
	v_pk_mul_f16 v153, v79, v57 op_sel:[1,0] op_sel_hi:[1,1]
	v_pk_mul_f16 v154, v79, v58 op_sel:[1,0] op_sel_hi:[1,1]
	v_pk_mul_f16 v155, v79, v59 op_sel:[1,0] op_sel_hi:[1,1]
	v_mfma_f32_32x32x16_f16 v[0:15], v[144:147], v[116:119], v[0:15]
	v_pk_fma_f16 v152, v71, v60, v152 op_sel:[1,0,0] op_sel_hi:[1,1,1]
	v_pk_fma_f16 v153, v71, v61, v153 op_sel:[1,0,0] op_sel_hi:[1,1,1]
	v_pk_fma_f16 v154, v71, v62, v154 op_sel:[1,0,0] op_sel_hi:[1,1,1]
	v_pk_fma_f16 v155, v71, v63, v155 op_sel:[1,0,0] op_sel_hi:[1,1,1]
	v_mfma_f32_32x32x16_f16 v[16:31], v[148:151], v[120:123], v[16:31]
	v_pk_mul_f16 v156, v79, v60 op_sel:[1,0] op_sel_hi:[1,1]
	v_pk_mul_f16 v157, v79, v61 op_sel:[1,0] op_sel_hi:[1,1]
	v_pk_mul_f16 v158, v79, v62 op_sel:[1,0] op_sel_hi:[1,1]
	v_pk_mul_f16 v159, v79, v63 op_sel:[1,0] op_sel_hi:[1,1]
	v_mfma_f32_32x32x16_f16 v[0:15], v[148:151], v[124:127], v[0:15]
	v_pk_fma_f16 v156, v71, v56, v156 op_sel:[1,0,0] op_sel_hi:[1,1,1] neg_lo:[0,0,1] neg_hi:[0,0,1]
	v_pk_fma_f16 v157, v71, v57, v157 op_sel:[1,0,0] op_sel_hi:[1,1,1] neg_lo:[0,0,1] neg_hi:[0,0,1]
	v_pk_fma_f16 v158, v71, v58, v158 op_sel:[1,0,0] op_sel_hi:[1,1,1] neg_lo:[0,0,1] neg_hi:[0,0,1]
	v_pk_fma_f16 v159, v71, v59, v159 op_sel:[1,0,0] op_sel_hi:[1,1,1] neg_lo:[0,0,1] neg_hi:[0,0,1]
	ds_read_b128 v[80:83], v161
	ds_read_b128 v[84:87], v161 offset:1024
	ds_read_b128 v[88:91], v161 offset:2048
	ds_read_b128 v[92:95], v161 offset:3072
	s_waitcnt lgkmcnt(4)
	v_mfma_f32_32x32x16_f16 v[16:31], v[152:155], v[128:131], v[16:31]
	s_waitcnt vmcnt(6)
	v_pk_mul_f16 v144, v48, v32 op_sel:[0,0] op_sel_hi:[0,1]
	v_pk_mul_f16 v145, v48, v33 op_sel:[0,0] op_sel_hi:[0,1]
	v_pk_mul_f16 v146, v48, v34 op_sel:[0,0] op_sel_hi:[0,1]
	v_pk_mul_f16 v147, v48, v35 op_sel:[0,0] op_sel_hi:[0,1]
	v_mfma_f32_32x32x16_f16 v[0:15], v[152:155], v[132:135], v[0:15]
	v_pk_fma_f16 v144, v40, v36, v144 op_sel:[0,0,0] op_sel_hi:[0,1,1]
	v_pk_fma_f16 v145, v40, v37, v145 op_sel:[0,0,0] op_sel_hi:[0,1,1]
	v_pk_fma_f16 v146, v40, v38, v146 op_sel:[0,0,0] op_sel_hi:[0,1,1]
	v_pk_fma_f16 v147, v40, v39, v147 op_sel:[0,0,0] op_sel_hi:[0,1,1]
	v_mfma_f32_32x32x16_f16 v[16:31], v[156:159], v[136:139], v[16:31]
	v_pk_mul_f16 v148, v48, v36 op_sel:[0,0] op_sel_hi:[0,1]
	v_pk_mul_f16 v149, v48, v37 op_sel:[0,0] op_sel_hi:[0,1]
	v_pk_mul_f16 v150, v48, v38 op_sel:[0,0] op_sel_hi:[0,1]
	v_pk_mul_f16 v151, v48, v39 op_sel:[0,0] op_sel_hi:[0,1]
	v_mfma_f32_32x32x16_f16 v[0:15], v[156:159], v[140:143], v[0:15]
	v_pk_fma_f16 v148, v40, v32, v148 op_sel:[0,0,0] op_sel_hi:[0,1,1] neg_lo:[0,0,1] neg_hi:[0,0,1]
	v_pk_fma_f16 v149, v40, v33, v149 op_sel:[0,0,0] op_sel_hi:[0,1,1] neg_lo:[0,0,1] neg_hi:[0,0,1]
	v_pk_fma_f16 v150, v40, v34, v150 op_sel:[0,0,0] op_sel_hi:[0,1,1] neg_lo:[0,0,1] neg_hi:[0,0,1]
	v_pk_fma_f16 v151, v40, v35, v151 op_sel:[0,0,0] op_sel_hi:[0,1,1] neg_lo:[0,0,1] neg_hi:[0,0,1]
	ds_read_b128 v[96:99], v161 offset:4096
	ds_read_b128 v[100:103], v161 offset:5120
	ds_read_b128 v[104:107], v161 offset:6144
	ds_read_b128 v[108:111], v161 offset:7168
	s_add_u32 s17, s17, 1
	s_cmp_eq_u32 s17, 17
	s_cbranch_scc1 .Lk2_epi
	s_branch .Lk2_s00
